# hand-written layer2 kernel (8-deep load ring, early self loads, exec-masked padded gathers) + sc1 output stores
# speedup vs baseline: 1.2732x; 1.0042x over previous
_Z12layer_kernelILb0ELi0EEvPKfPKDF16_PKhS3_PK15HIP_vector_typeIiLj4EEPKtPKiS3_S1_PvPhPDF16_:
	s_load_dwordx8 s[8:15], s[0:1], 0x0
	s_load_dwordx8 s[16:23], s[0:1], 0x20
	s_load_dwordx8 s[24:31], s[0:1], 0x40
	v_lshrrev_b32_e32 v94, 6, v0
	v_and_b32_e32 v1, 63, v0
	v_lshlrev_b32_e32 v95, 4, v0
	v_readfirstlane_b32 s3, v94
	s_and_b32 s4, s2, 7
	s_lshr_b32 s5, s2, 3
	s_lshl_b32 s7, s3, 5
	s_add_u32 s5, s5, s7
	s_movk_i32 s7, 0x185
	s_cmp_eq_u32 s4, 3
	s_cselect_b32 s7, s7, 0x180
	s_movk_i32 s58, 0x190
	s_cmp_lt_u32 s4, 3
	s_cselect_b32 s7, s58, s7
	s_lshr_b32 s6, s5, 4
	s_lshl_b32 s6, s6, 3
	s_add_u32 s6, s6, s4
	s_lshl_b32 s6, s6, 4
	s_and_b32 s58, s5, 15
	s_add_u32 s6, s6, s58
	v_lshrrev_b32_e32 v96, 5, v0
	v_and_b32_e32 v97, 31, v0
	v_and_b32_e32 v98, 15, v96
	v_xor_b32_e32 v97, v97, v98
	v_lshlrev_b32_e32 v97, 4, v97
	v_lshl_or_b32 v96, v96, 9, v97
	v_add_u32_e32 v98, 0x4000, v95
	v_add_u32_e32 v99, 0x8000, v95
	v_add_u32_e32 v100, 0xc000, v95
	s_cmp_lt_u32 s5, s7
	s_cbranch_scc1 .Lg2_active
	s_waitcnt lgkmcnt(0)
	global_load_dwordx4 v[2:5], v95, s[22:23]
	global_load_dwordx4 v[6:9], v98, s[22:23]
	global_load_dwordx4 v[10:13], v99, s[22:23]
	global_load_dwordx4 v[14:17], v100, s[22:23]
	s_waitcnt vmcnt(0)
	ds_write_b128 v96, v[2:5]
	ds_write_b128 v96, v[6:9] offset:16384
	ds_write_b128 v96, v[10:13] offset:32768
	ds_write_b128 v96, v[14:17] offset:49152
	s_waitcnt lgkmcnt(0)
	s_barrier
	s_endpgm
.Lg2_active:
	s_mov_b32 s60, 0x00ff00ff
	s_mov_b32 s61, 0x0c030c01
	v_lshrrev_b32_e32 v107, 3, v1
	v_and_b32_e32 v108, 7, v1
	v_and_b32_e32 v105, 15, v1
	v_lshrrev_b32_e32 v106, 4, v1
	s_bfe_u32 s36, s3, 0x10002
	s_lshl_b32 s58, s36, 3
	s_xor_b32 s59, s58, 8
	v_or_b32_e32 v102, s58, v107
	v_or_b32_e32 v103, s59, v107
	v_lshlrev_b32_e32 v89, 4, v108
	v_and_b32_e32 v90, 56, v1
	v_lshlrev_b32_e32 v90, 2, v90
	s_waitcnt lgkmcnt(0)
	s_lshl_b32 s58, s6, 8
	s_add_u32 s32, s16, s58
	s_addc_u32 s33, s17, 0
	s_lshl_b32 s58, s6, 10
	s_add_u32 s34, s18, s58
	s_addc_u32 s35, s19, 0
	v_lshlrev_b32_e32 v109, 4, v105
	global_load_dword v104, v109, s[32:33] offset:8
	v_lshlrev_b32_e32 v110, 4, v102
	global_load_dwordx2 v[68:69], v110, s[32:33]
	v_lshlrev_b32_e32 v111, 4, v103
	global_load_dwordx2 v[70:71], v111, s[32:33]
	v_lshlrev_b32_e32 v101, 2, v108
	v_lshl_or_b32 v110, v102, 6, v101
	global_load_dword v60, v110, s[34:35]
	global_load_dword v61, v110, s[34:35] offset:32
	v_lshl_or_b32 v111, v103, 6, v101
	global_load_dword v62, v111, s[34:35]
	global_load_dword v63, v111, s[34:35] offset:32
	global_load_dwordx4 v[2:5], v95, s[22:23]
	global_load_dwordx4 v[6:9], v98, s[22:23]
	global_load_dwordx4 v[10:13], v99, s[22:23]
	global_load_dwordx4 v[14:17], v100, s[22:23]
	v_and_b32_e32 v101, 0x7f, v0
	v_lshlrev_b32_e32 v101, 2, v101
	global_load_dword v19, v101, s[24:25]
	s_mul_i32 s48, s3, 0x1100
	s_add_u32 s48, s48, 0x10200
	v_mul_u32_u24_e32 v91, 0x110, v102
	v_lshl_add_u32 v91, v108, 5, v91
	v_add_u32_e32 v91, s48, v91
	v_mul_u32_u24_e32 v92, 0x110, v103
	v_lshl_add_u32 v92, v108, 5, v92
	v_add_u32_e32 v92, s48, v92
	s_waitcnt vmcnt(5)
	v_readlane_b32 s49, v69, 0
	v_readlane_b32 s50, v69, 8
	v_readlane_b32 s51, v69, 16
	v_readlane_b32 s52, v69, 24
	v_readlane_b32 s53, v69, 32
	v_readlane_b32 s54, v69, 40
	v_readlane_b32 s55, v69, 48
	v_readlane_b32 s56, v69, 56
	s_max_i32 s37, s49, s50
	s_max_i32 s37, s37, s51
	s_max_i32 s37, s37, s52
	s_max_i32 s37, s37, s53
	s_max_i32 s37, s37, s54
	s_max_i32 s37, s37, s55
	s_max_i32 s37, s37, s56
	v_readlane_b32 s49, v71, 0
	v_readlane_b32 s50, v71, 8
	v_readlane_b32 s51, v71, 16
	v_readlane_b32 s52, v71, 24
	v_readlane_b32 s53, v71, 32
	v_readlane_b32 s54, v71, 40
	v_readlane_b32 s55, v71, 48
	v_readlane_b32 s56, v71, 56
	s_max_i32 s38, s49, s50
	s_max_i32 s38, s38, s51
	s_max_i32 s38, s38, s52
	s_max_i32 s38, s38, s53
	s_max_i32 s38, s38, s54
	s_max_i32 s38, s38, s55
	s_max_i32 s38, s38, s56
	v_and_b32_e32 v103, 0xffff, v60
	v_lshlrev_b32_e32 v103, 1, v103
	global_load_ushort v20, v103, s[14:15]
	v_lshrrev_b32_e32 v109, 16, v60
	v_lshlrev_b32_e32 v109, 1, v109
	global_load_ushort v21, v109, s[14:15]
	v_and_b32_e32 v103, 0xffff, v61
	v_lshlrev_b32_e32 v103, 1, v103
	global_load_ushort v22, v103, s[14:15]
	v_lshrrev_b32_e32 v109, 16, v61
	v_lshlrev_b32_e32 v109, 1, v109
	global_load_ushort v23, v109, s[14:15]
	v_and_b32_e32 v103, 0xffff, v62
	v_lshlrev_b32_e32 v103, 1, v103
	global_load_ushort v24, v103, s[14:15]
	v_lshrrev_b32_e32 v109, 16, v62
	v_lshlrev_b32_e32 v109, 1, v109
	global_load_ushort v25, v109, s[14:15]
	v_and_b32_e32 v103, 0xffff, v63
	v_lshlrev_b32_e32 v103, 1, v103
	global_load_ushort v26, v103, s[14:15]
	v_lshrrev_b32_e32 v109, 16, v63
	v_lshlrev_b32_e32 v109, 1, v109
	global_load_ushort v27, v109, s[14:15]
	v_lshlrev_b32_e32 v102, 8, v104
	v_lshl_or_b32 v102, v106, 4, v102
	global_load_dwordx4 v[112:115], v102, s[10:11] offset:0
	global_load_dwordx4 v[116:119], v102, s[10:11] offset:64
	global_load_dwordx4 v[120:123], v102, s[10:11] offset:128
	global_load_dwordx4 v[124:127], v102, s[10:11] offset:192
	s_waitcnt vmcnt(12)
	ds_write_b128 v96, v[2:5]
	ds_write_b128 v96, v[6:9] offset:16384
	ds_write_b128 v96, v[10:13] offset:32768
	ds_write_b128 v96, v[14:17] offset:49152
	v_add_u32_e32 v101, 0x10000, v101
	ds_write_b32 v101, v19
	s_waitcnt lgkmcnt(0)
	s_barrier
	s_mov_b32 s39, 0
	s_waitcnt vmcnt(4)
	v_lshl_or_b32 v64, v21, 16, v20
	v_lshl_or_b32 v65, v23, 16, v22
	v_lshl_or_b32 v66, v25, 16, v24
	v_lshl_or_b32 v67, v27, 16, v26
.Lg2_set_top:
	s_cmp_eq_u32 s39, 0
	s_cbranch_scc0 .Lg2_sel_b
	v_mov_b32_e32 v73, v60
	v_mov_b32_e32 v74, v61
	v_mov_b32_e32 v75, v64
	v_mov_b32_e32 v76, v65
	v_mov_b32_e32 v77, v68
	v_mov_b32_e32 v78, v69
	v_mov_b32_e32 v93, v91
	s_mov_b32 s41, s37
	s_branch .Lg2_sel_done
.Lg2_sel_b:
	v_mov_b32_e32 v73, v62
	v_mov_b32_e32 v74, v63
	v_mov_b32_e32 v75, v66
	v_mov_b32_e32 v76, v67
	v_mov_b32_e32 v77, v70
	v_mov_b32_e32 v78, v71
	v_mov_b32_e32 v93, v92
	s_mov_b32 s41, s38
.Lg2_sel_done:
	s_min_i32 s40, s41, 32
	s_add_i32 s40, s40, 3
	s_and_b32 s40, s40, 0x3c
	s_max_i32 s40, s40, 8
	v_mov_b32_e32 v2, 0
	v_mov_b32_e32 v3, 0
	v_mov_b32_e32 v4, 0
	v_mov_b32_e32 v5, 0
	v_mov_b32_e32 v6, 0
	v_mov_b32_e32 v7, 0
	v_mov_b32_e32 v8, 0
	v_mov_b32_e32 v9, 0
	v_mov_b32_e32 v10, 0
	v_mov_b32_e32 v11, 0
	v_mov_b32_e32 v12, 0
	v_mov_b32_e32 v13, 0
	v_mov_b32_e32 v14, 0
	v_mov_b32_e32 v15, 0
	v_mov_b32_e32 v16, 0
	v_mov_b32_e32 v17, 0
	s_waitcnt lgkmcnt(0)
	ds_bpermute_b32 v94, v90, v73 offset:0
	ds_bpermute_b32 v98, v90, v75 offset:0
	ds_bpermute_b32 v95, v90, v73 offset:4
	ds_bpermute_b32 v99, v90, v75 offset:4
	ds_bpermute_b32 v96, v90, v73 offset:8
	ds_bpermute_b32 v100, v90, v75 offset:8
	ds_bpermute_b32 v97, v90, v73 offset:12
	ds_bpermute_b32 v101, v90, v75 offset:12
	ds_bpermute_b32 v79, v90, v73 offset:16
	ds_bpermute_b32 v81, v90, v75 offset:16
	s_waitcnt lgkmcnt(2)
	v_and_b32_e32 v84, 0xffff, v94
	v_lshl_or_b32 v83, v84, 7, v89
	v_cmp_lt_i32_e32 vcc, 0, v78
	s_mov_b64 exec, vcc
	global_load_dwordx4 v[20:23], v83, s[12:13]
	s_mov_b64 exec, -1
	v_cvt_f32_f16_e32 v52, v98
	v_lshrrev_b32_e32 v84, 16, v94
	v_lshl_or_b32 v83, v84, 7, v89
	v_cmp_lt_i32_e32 vcc, 1, v78
	s_mov_b64 exec, vcc
	global_load_dwordx4 v[24:27], v83, s[12:13]
	s_mov_b64 exec, -1
	v_cvt_f32_f16_sdwa v53, v98 dst_sel:DWORD dst_unused:UNUSED_PAD src0_sel:WORD_1
	v_and_b32_e32 v84, 0xffff, v95
	v_lshl_or_b32 v83, v84, 7, v89
	v_cmp_lt_i32_e32 vcc, 2, v78
	s_mov_b64 exec, vcc
	global_load_dwordx4 v[28:31], v83, s[12:13]
	s_mov_b64 exec, -1
	v_cvt_f32_f16_e32 v54, v99
	v_lshrrev_b32_e32 v84, 16, v95
	v_lshl_or_b32 v83, v84, 7, v89
	v_cmp_lt_i32_e32 vcc, 3, v78
	s_mov_b64 exec, vcc
	global_load_dwordx4 v[32:35], v83, s[12:13]
	s_mov_b64 exec, -1
	v_cvt_f32_f16_sdwa v55, v99 dst_sel:DWORD dst_unused:UNUSED_PAD src0_sel:WORD_1
	v_and_b32_e32 v84, 0xffff, v96
	v_lshl_or_b32 v83, v84, 7, v89
	v_cmp_lt_i32_e32 vcc, 4, v78
	s_mov_b64 exec, vcc
	global_load_dwordx4 v[36:39], v83, s[12:13]
	s_mov_b64 exec, -1
	v_cvt_f32_f16_e32 v56, v100
	v_lshrrev_b32_e32 v84, 16, v96
	v_lshl_or_b32 v83, v84, 7, v89
	v_cmp_lt_i32_e32 vcc, 5, v78
	s_mov_b64 exec, vcc
	global_load_dwordx4 v[40:43], v83, s[12:13]
	s_mov_b64 exec, -1
	v_cvt_f32_f16_sdwa v57, v100 dst_sel:DWORD dst_unused:UNUSED_PAD src0_sel:WORD_1
	v_and_b32_e32 v84, 0xffff, v97
	v_lshl_or_b32 v83, v84, 7, v89
	v_cmp_lt_i32_e32 vcc, 6, v78
	s_mov_b64 exec, vcc
	global_load_dwordx4 v[44:47], v83, s[12:13]
	s_mov_b64 exec, -1
	v_cvt_f32_f16_e32 v58, v101
	v_lshrrev_b32_e32 v84, 16, v97
	v_lshl_or_b32 v83, v84, 7, v89
	v_cmp_lt_i32_e32 vcc, 7, v78
	s_mov_b64 exec, vcc
	global_load_dwordx4 v[48:51], v83, s[12:13]
	s_mov_b64 exec, -1
	v_cvt_f32_f16_sdwa v59, v101 dst_sel:DWORD dst_unused:UNUSED_PAD src0_sel:WORD_1
	s_cmp_le_u32 s40, 8
	s_cbranch_scc1 .Lg2_tail0
	s_waitcnt lgkmcnt(0)
	ds_bpermute_b32 v80, v90, v73 offset:20
	ds_bpermute_b32 v82, v90, v75 offset:20
	s_waitcnt vmcnt(7)
	v_cvt_f32_ubyte0_e32 v85, v20
	v_cvt_f32_ubyte1_e32 v86, v20
	v_cvt_f32_ubyte2_e32 v87, v20
	v_cvt_f32_ubyte3_e32 v88, v20
	v_fmac_f32_e32 v2, v85, v52
	v_fmac_f32_e32 v3, v86, v52
	v_fmac_f32_e32 v4, v87, v52
	v_fmac_f32_e32 v5, v88, v52
	v_cvt_f32_ubyte0_e32 v85, v21
	v_cvt_f32_ubyte1_e32 v86, v21
	v_cvt_f32_ubyte2_e32 v87, v21
	v_cvt_f32_ubyte3_e32 v88, v21
	v_fmac_f32_e32 v6, v85, v52
	v_fmac_f32_e32 v7, v86, v52
	v_fmac_f32_e32 v8, v87, v52
	v_fmac_f32_e32 v9, v88, v52
	v_cvt_f32_ubyte0_e32 v85, v22
	v_cvt_f32_ubyte1_e32 v86, v22
	v_cvt_f32_ubyte2_e32 v87, v22
	v_cvt_f32_ubyte3_e32 v88, v22
	v_fmac_f32_e32 v10, v85, v52
	v_fmac_f32_e32 v11, v86, v52
	v_fmac_f32_e32 v12, v87, v52
	v_fmac_f32_e32 v13, v88, v52
	v_cvt_f32_ubyte0_e32 v85, v23
	v_cvt_f32_ubyte1_e32 v86, v23
	v_cvt_f32_ubyte2_e32 v87, v23
	v_cvt_f32_ubyte3_e32 v88, v23
	v_fmac_f32_e32 v14, v85, v52
	v_fmac_f32_e32 v15, v86, v52
	v_fmac_f32_e32 v16, v87, v52
	v_fmac_f32_e32 v17, v88, v52
	v_and_b32_e32 v84, 0xffff, v79
	v_lshl_or_b32 v83, v84, 7, v89
	v_cmp_lt_i32_e32 vcc, 8, v78
	s_mov_b64 exec, vcc
	global_load_dwordx4 v[20:23], v83, s[12:13]
	s_mov_b64 exec, -1
	v_cvt_f32_f16_e32 v52, v81
	s_waitcnt vmcnt(7)
	v_cvt_f32_ubyte0_e32 v85, v24
	v_cvt_f32_ubyte1_e32 v86, v24
	v_cvt_f32_ubyte2_e32 v87, v24
	v_cvt_f32_ubyte3_e32 v88, v24
	v_fmac_f32_e32 v2, v85, v53
	v_fmac_f32_e32 v3, v86, v53
	v_fmac_f32_e32 v4, v87, v53
	v_fmac_f32_e32 v5, v88, v53
	v_cvt_f32_ubyte0_e32 v85, v25
	v_cvt_f32_ubyte1_e32 v86, v25
	v_cvt_f32_ubyte2_e32 v87, v25
	v_cvt_f32_ubyte3_e32 v88, v25
	v_fmac_f32_e32 v6, v85, v53
	v_fmac_f32_e32 v7, v86, v53
	v_fmac_f32_e32 v8, v87, v53
	v_fmac_f32_e32 v9, v88, v53
	v_cvt_f32_ubyte0_e32 v85, v26
	v_cvt_f32_ubyte1_e32 v86, v26
	v_cvt_f32_ubyte2_e32 v87, v26
	v_cvt_f32_ubyte3_e32 v88, v26
	v_fmac_f32_e32 v10, v85, v53
	v_fmac_f32_e32 v11, v86, v53
	v_fmac_f32_e32 v12, v87, v53
	v_fmac_f32_e32 v13, v88, v53
	v_cvt_f32_ubyte0_e32 v85, v27
	v_cvt_f32_ubyte1_e32 v86, v27
	v_cvt_f32_ubyte2_e32 v87, v27
	v_cvt_f32_ubyte3_e32 v88, v27
	v_fmac_f32_e32 v14, v85, v53
	v_fmac_f32_e32 v15, v86, v53
	v_fmac_f32_e32 v16, v87, v53
	v_fmac_f32_e32 v17, v88, v53
	v_lshrrev_b32_e32 v84, 16, v79
	v_lshl_or_b32 v83, v84, 7, v89
	v_cmp_lt_i32_e32 vcc, 9, v78
	s_mov_b64 exec, vcc
	global_load_dwordx4 v[24:27], v83, s[12:13]
	s_mov_b64 exec, -1
	v_cvt_f32_f16_sdwa v53, v81 dst_sel:DWORD dst_unused:UNUSED_PAD src0_sel:WORD_1
	s_waitcnt lgkmcnt(0)
	ds_bpermute_b32 v79, v90, v73 offset:24
	ds_bpermute_b32 v81, v90, v75 offset:24
	s_waitcnt vmcnt(7)
	v_cvt_f32_ubyte0_e32 v85, v28
	v_cvt_f32_ubyte1_e32 v86, v28
	v_cvt_f32_ubyte2_e32 v87, v28
	v_cvt_f32_ubyte3_e32 v88, v28
	v_fmac_f32_e32 v2, v85, v54
	v_fmac_f32_e32 v3, v86, v54
	v_fmac_f32_e32 v4, v87, v54
	v_fmac_f32_e32 v5, v88, v54
	v_cvt_f32_ubyte0_e32 v85, v29
	v_cvt_f32_ubyte1_e32 v86, v29
	v_cvt_f32_ubyte2_e32 v87, v29
	v_cvt_f32_ubyte3_e32 v88, v29
	v_fmac_f32_e32 v6, v85, v54
	v_fmac_f32_e32 v7, v86, v54
	v_fmac_f32_e32 v8, v87, v54
	v_fmac_f32_e32 v9, v88, v54
	v_cvt_f32_ubyte0_e32 v85, v30
	v_cvt_f32_ubyte1_e32 v86, v30
	v_cvt_f32_ubyte2_e32 v87, v30
	v_cvt_f32_ubyte3_e32 v88, v30
	v_fmac_f32_e32 v10, v85, v54
	v_fmac_f32_e32 v11, v86, v54
	v_fmac_f32_e32 v12, v87, v54
	v_fmac_f32_e32 v13, v88, v54
	v_cvt_f32_ubyte0_e32 v85, v31
	v_cvt_f32_ubyte1_e32 v86, v31
	v_cvt_f32_ubyte2_e32 v87, v31
	v_cvt_f32_ubyte3_e32 v88, v31
	v_fmac_f32_e32 v14, v85, v54
	v_fmac_f32_e32 v15, v86, v54
	v_fmac_f32_e32 v16, v87, v54
	v_fmac_f32_e32 v17, v88, v54
	v_and_b32_e32 v84, 0xffff, v80
	v_lshl_or_b32 v83, v84, 7, v89
	v_cmp_lt_i32_e32 vcc, 10, v78
	s_mov_b64 exec, vcc
	global_load_dwordx4 v[28:31], v83, s[12:13]
	s_mov_b64 exec, -1
	v_cvt_f32_f16_e32 v54, v82
	s_waitcnt vmcnt(7)
	v_cvt_f32_ubyte0_e32 v85, v32
	v_cvt_f32_ubyte1_e32 v86, v32
	v_cvt_f32_ubyte2_e32 v87, v32
	v_cvt_f32_ubyte3_e32 v88, v32
	v_fmac_f32_e32 v2, v85, v55
	v_fmac_f32_e32 v3, v86, v55
	v_fmac_f32_e32 v4, v87, v55
	v_fmac_f32_e32 v5, v88, v55
	v_cvt_f32_ubyte0_e32 v85, v33
	v_cvt_f32_ubyte1_e32 v86, v33
	v_cvt_f32_ubyte2_e32 v87, v33
	v_cvt_f32_ubyte3_e32 v88, v33
	v_fmac_f32_e32 v6, v85, v55
	v_fmac_f32_e32 v7, v86, v55
	v_fmac_f32_e32 v8, v87, v55
	v_fmac_f32_e32 v9, v88, v55
	v_cvt_f32_ubyte0_e32 v85, v34
	v_cvt_f32_ubyte1_e32 v86, v34
	v_cvt_f32_ubyte2_e32 v87, v34
	v_cvt_f32_ubyte3_e32 v88, v34
	v_fmac_f32_e32 v10, v85, v55
	v_fmac_f32_e32 v11, v86, v55
	v_fmac_f32_e32 v12, v87, v55
	v_fmac_f32_e32 v13, v88, v55
	v_cvt_f32_ubyte0_e32 v85, v35
	v_cvt_f32_ubyte1_e32 v86, v35
	v_cvt_f32_ubyte2_e32 v87, v35
	v_cvt_f32_ubyte3_e32 v88, v35
	v_fmac_f32_e32 v14, v85, v55
	v_fmac_f32_e32 v15, v86, v55
	v_fmac_f32_e32 v16, v87, v55
	v_fmac_f32_e32 v17, v88, v55
	v_lshrrev_b32_e32 v84, 16, v80
	v_lshl_or_b32 v83, v84, 7, v89
	v_cmp_lt_i32_e32 vcc, 11, v78
	s_mov_b64 exec, vcc
	global_load_dwordx4 v[32:35], v83, s[12:13]
	s_mov_b64 exec, -1
	v_cvt_f32_f16_sdwa v55, v82 dst_sel:DWORD dst_unused:UNUSED_PAD src0_sel:WORD_1
	s_cmp_le_u32 s40, 12
	s_cbranch_scc1 .Lg2_tail4
	s_waitcnt lgkmcnt(0)
	ds_bpermute_b32 v80, v90, v73 offset:28
	ds_bpermute_b32 v82, v90, v75 offset:28
	s_waitcnt vmcnt(7)
	v_cvt_f32_ubyte0_e32 v85, v36
	v_cvt_f32_ubyte1_e32 v86, v36
	v_cvt_f32_ubyte2_e32 v87, v36
	v_cvt_f32_ubyte3_e32 v88, v36
	v_fmac_f32_e32 v2, v85, v56
	v_fmac_f32_e32 v3, v86, v56
	v_fmac_f32_e32 v4, v87, v56
	v_fmac_f32_e32 v5, v88, v56
	v_cvt_f32_ubyte0_e32 v85, v37
	v_cvt_f32_ubyte1_e32 v86, v37
	v_cvt_f32_ubyte2_e32 v87, v37
	v_cvt_f32_ubyte3_e32 v88, v37
	v_fmac_f32_e32 v6, v85, v56
	v_fmac_f32_e32 v7, v86, v56
	v_fmac_f32_e32 v8, v87, v56
	v_fmac_f32_e32 v9, v88, v56
	v_cvt_f32_ubyte0_e32 v85, v38
	v_cvt_f32_ubyte1_e32 v86, v38
	v_cvt_f32_ubyte2_e32 v87, v38
	v_cvt_f32_ubyte3_e32 v88, v38
	v_fmac_f32_e32 v10, v85, v56
	v_fmac_f32_e32 v11, v86, v56
	v_fmac_f32_e32 v12, v87, v56
	v_fmac_f32_e32 v13, v88, v56
	v_cvt_f32_ubyte0_e32 v85, v39
	v_cvt_f32_ubyte1_e32 v86, v39
	v_cvt_f32_ubyte2_e32 v87, v39
	v_cvt_f32_ubyte3_e32 v88, v39
	v_fmac_f32_e32 v14, v85, v56
	v_fmac_f32_e32 v15, v86, v56
	v_fmac_f32_e32 v16, v87, v56
	v_fmac_f32_e32 v17, v88, v56
	v_and_b32_e32 v84, 0xffff, v79
	v_lshl_or_b32 v83, v84, 7, v89
	v_cmp_lt_i32_e32 vcc, 12, v78
	s_mov_b64 exec, vcc
	global_load_dwordx4 v[36:39], v83, s[12:13]
	s_mov_b64 exec, -1
	v_cvt_f32_f16_e32 v56, v81
	s_waitcnt vmcnt(7)
	v_cvt_f32_ubyte0_e32 v85, v40
	v_cvt_f32_ubyte1_e32 v86, v40
	v_cvt_f32_ubyte2_e32 v87, v40
	v_cvt_f32_ubyte3_e32 v88, v40
	v_fmac_f32_e32 v2, v85, v57
	v_fmac_f32_e32 v3, v86, v57
	v_fmac_f32_e32 v4, v87, v57
	v_fmac_f32_e32 v5, v88, v57
	v_cvt_f32_ubyte0_e32 v85, v41
	v_cvt_f32_ubyte1_e32 v86, v41
	v_cvt_f32_ubyte2_e32 v87, v41
	v_cvt_f32_ubyte3_e32 v88, v41
	v_fmac_f32_e32 v6, v85, v57
	v_fmac_f32_e32 v7, v86, v57
	v_fmac_f32_e32 v8, v87, v57
	v_fmac_f32_e32 v9, v88, v57
	v_cvt_f32_ubyte0_e32 v85, v42
	v_cvt_f32_ubyte1_e32 v86, v42
	v_cvt_f32_ubyte2_e32 v87, v42
	v_cvt_f32_ubyte3_e32 v88, v42
	v_fmac_f32_e32 v10, v85, v57
	v_fmac_f32_e32 v11, v86, v57
	v_fmac_f32_e32 v12, v87, v57
	v_fmac_f32_e32 v13, v88, v57
	v_cvt_f32_ubyte0_e32 v85, v43
	v_cvt_f32_ubyte1_e32 v86, v43
	v_cvt_f32_ubyte2_e32 v87, v43
	v_cvt_f32_ubyte3_e32 v88, v43
	v_fmac_f32_e32 v14, v85, v57
	v_fmac_f32_e32 v15, v86, v57
	v_fmac_f32_e32 v16, v87, v57
	v_fmac_f32_e32 v17, v88, v57
	v_lshrrev_b32_e32 v84, 16, v79
	v_lshl_or_b32 v83, v84, 7, v89
	v_cmp_lt_i32_e32 vcc, 13, v78
	s_mov_b64 exec, vcc
	global_load_dwordx4 v[40:43], v83, s[12:13]
	s_mov_b64 exec, -1
	v_cvt_f32_f16_sdwa v57, v81 dst_sel:DWORD dst_unused:UNUSED_PAD src0_sel:WORD_1
	s_waitcnt lgkmcnt(0)
	ds_bpermute_b32 v79, v90, v74 offset:0
	ds_bpermute_b32 v81, v90, v76 offset:0
	s_waitcnt vmcnt(7)
	v_cvt_f32_ubyte0_e32 v85, v44
	v_cvt_f32_ubyte1_e32 v86, v44
	v_cvt_f32_ubyte2_e32 v87, v44
	v_cvt_f32_ubyte3_e32 v88, v44
	v_fmac_f32_e32 v2, v85, v58
	v_fmac_f32_e32 v3, v86, v58
	v_fmac_f32_e32 v4, v87, v58
	v_fmac_f32_e32 v5, v88, v58
	v_cvt_f32_ubyte0_e32 v85, v45
	v_cvt_f32_ubyte1_e32 v86, v45
	v_cvt_f32_ubyte2_e32 v87, v45
	v_cvt_f32_ubyte3_e32 v88, v45
	v_fmac_f32_e32 v6, v85, v58
	v_fmac_f32_e32 v7, v86, v58
	v_fmac_f32_e32 v8, v87, v58
	v_fmac_f32_e32 v9, v88, v58
	v_cvt_f32_ubyte0_e32 v85, v46
	v_cvt_f32_ubyte1_e32 v86, v46
	v_cvt_f32_ubyte2_e32 v87, v46
	v_cvt_f32_ubyte3_e32 v88, v46
	v_fmac_f32_e32 v10, v85, v58
	v_fmac_f32_e32 v11, v86, v58
	v_fmac_f32_e32 v12, v87, v58
	v_fmac_f32_e32 v13, v88, v58
	v_cvt_f32_ubyte0_e32 v85, v47
	v_cvt_f32_ubyte1_e32 v86, v47
	v_cvt_f32_ubyte2_e32 v87, v47
	v_cvt_f32_ubyte3_e32 v88, v47
	v_fmac_f32_e32 v14, v85, v58
	v_fmac_f32_e32 v15, v86, v58
	v_fmac_f32_e32 v16, v87, v58
	v_fmac_f32_e32 v17, v88, v58
	v_and_b32_e32 v84, 0xffff, v80
	v_lshl_or_b32 v83, v84, 7, v89
	v_cmp_lt_i32_e32 vcc, 14, v78
	s_mov_b64 exec, vcc
	global_load_dwordx4 v[44:47], v83, s[12:13]
	s_mov_b64 exec, -1
	v_cvt_f32_f16_e32 v58, v82
	s_waitcnt vmcnt(7)
	v_cvt_f32_ubyte0_e32 v85, v48
	v_cvt_f32_ubyte1_e32 v86, v48
	v_cvt_f32_ubyte2_e32 v87, v48
	v_cvt_f32_ubyte3_e32 v88, v48
	v_fmac_f32_e32 v2, v85, v59
	v_fmac_f32_e32 v3, v86, v59
	v_fmac_f32_e32 v4, v87, v59
	v_fmac_f32_e32 v5, v88, v59
	v_cvt_f32_ubyte0_e32 v85, v49
	v_cvt_f32_ubyte1_e32 v86, v49
	v_cvt_f32_ubyte2_e32 v87, v49
	v_cvt_f32_ubyte3_e32 v88, v49
	v_fmac_f32_e32 v6, v85, v59
	v_fmac_f32_e32 v7, v86, v59
	v_fmac_f32_e32 v8, v87, v59
	v_fmac_f32_e32 v9, v88, v59
	v_cvt_f32_ubyte0_e32 v85, v50
	v_cvt_f32_ubyte1_e32 v86, v50
	v_cvt_f32_ubyte2_e32 v87, v50
	v_cvt_f32_ubyte3_e32 v88, v50
	v_fmac_f32_e32 v10, v85, v59
	v_fmac_f32_e32 v11, v86, v59
	v_fmac_f32_e32 v12, v87, v59
	v_fmac_f32_e32 v13, v88, v59
	v_cvt_f32_ubyte0_e32 v85, v51
	v_cvt_f32_ubyte1_e32 v86, v51
	v_cvt_f32_ubyte2_e32 v87, v51
	v_cvt_f32_ubyte3_e32 v88, v51
	v_fmac_f32_e32 v14, v85, v59
	v_fmac_f32_e32 v15, v86, v59
	v_fmac_f32_e32 v16, v87, v59
	v_fmac_f32_e32 v17, v88, v59
	v_lshrrev_b32_e32 v84, 16, v80
	v_lshl_or_b32 v83, v84, 7, v89
	v_cmp_lt_i32_e32 vcc, 15, v78
	s_mov_b64 exec, vcc
	global_load_dwordx4 v[48:51], v83, s[12:13]
	s_mov_b64 exec, -1
	v_cvt_f32_f16_sdwa v59, v82 dst_sel:DWORD dst_unused:UNUSED_PAD src0_sel:WORD_1
	s_cmp_le_u32 s40, 16
	s_cbranch_scc1 .Lg2_tail0
	s_waitcnt lgkmcnt(0)
	ds_bpermute_b32 v80, v90, v74 offset:4
	ds_bpermute_b32 v82, v90, v76 offset:4
	s_waitcnt vmcnt(7)
	v_cvt_f32_ubyte0_e32 v85, v20
	v_cvt_f32_ubyte1_e32 v86, v20
	v_cvt_f32_ubyte2_e32 v87, v20
	v_cvt_f32_ubyte3_e32 v88, v20
	v_fmac_f32_e32 v2, v85, v52
	v_fmac_f32_e32 v3, v86, v52
	v_fmac_f32_e32 v4, v87, v52
	v_fmac_f32_e32 v5, v88, v52
	v_cvt_f32_ubyte0_e32 v85, v21
	v_cvt_f32_ubyte1_e32 v86, v21
	v_cvt_f32_ubyte2_e32 v87, v21
	v_cvt_f32_ubyte3_e32 v88, v21
	v_fmac_f32_e32 v6, v85, v52
	v_fmac_f32_e32 v7, v86, v52
	v_fmac_f32_e32 v8, v87, v52
	v_fmac_f32_e32 v9, v88, v52
	v_cvt_f32_ubyte0_e32 v85, v22
	v_cvt_f32_ubyte1_e32 v86, v22
	v_cvt_f32_ubyte2_e32 v87, v22
	v_cvt_f32_ubyte3_e32 v88, v22
	v_fmac_f32_e32 v10, v85, v52
	v_fmac_f32_e32 v11, v86, v52
	v_fmac_f32_e32 v12, v87, v52
	v_fmac_f32_e32 v13, v88, v52
	v_cvt_f32_ubyte0_e32 v85, v23
	v_cvt_f32_ubyte1_e32 v86, v23
	v_cvt_f32_ubyte2_e32 v87, v23
	v_cvt_f32_ubyte3_e32 v88, v23
	v_fmac_f32_e32 v14, v85, v52
	v_fmac_f32_e32 v15, v86, v52
	v_fmac_f32_e32 v16, v87, v52
	v_fmac_f32_e32 v17, v88, v52
	v_and_b32_e32 v84, 0xffff, v79
	v_lshl_or_b32 v83, v84, 7, v89
	v_cmp_lt_i32_e32 vcc, 16, v78
	s_mov_b64 exec, vcc
	global_load_dwordx4 v[20:23], v83, s[12:13]
	s_mov_b64 exec, -1
	v_cvt_f32_f16_e32 v52, v81
	s_waitcnt vmcnt(7)
	v_cvt_f32_ubyte0_e32 v85, v24
	v_cvt_f32_ubyte1_e32 v86, v24
	v_cvt_f32_ubyte2_e32 v87, v24
	v_cvt_f32_ubyte3_e32 v88, v24
	v_fmac_f32_e32 v2, v85, v53
	v_fmac_f32_e32 v3, v86, v53
	v_fmac_f32_e32 v4, v87, v53
	v_fmac_f32_e32 v5, v88, v53
	v_cvt_f32_ubyte0_e32 v85, v25
	v_cvt_f32_ubyte1_e32 v86, v25
	v_cvt_f32_ubyte2_e32 v87, v25
	v_cvt_f32_ubyte3_e32 v88, v25
	v_fmac_f32_e32 v6, v85, v53
	v_fmac_f32_e32 v7, v86, v53
	v_fmac_f32_e32 v8, v87, v53
	v_fmac_f32_e32 v9, v88, v53
	v_cvt_f32_ubyte0_e32 v85, v26
	v_cvt_f32_ubyte1_e32 v86, v26
	v_cvt_f32_ubyte2_e32 v87, v26
	v_cvt_f32_ubyte3_e32 v88, v26
	v_fmac_f32_e32 v10, v85, v53
	v_fmac_f32_e32 v11, v86, v53
	v_fmac_f32_e32 v12, v87, v53
	v_fmac_f32_e32 v13, v88, v53
	v_cvt_f32_ubyte0_e32 v85, v27
	v_cvt_f32_ubyte1_e32 v86, v27
	v_cvt_f32_ubyte2_e32 v87, v27
	v_cvt_f32_ubyte3_e32 v88, v27
	v_fmac_f32_e32 v14, v85, v53
	v_fmac_f32_e32 v15, v86, v53
	v_fmac_f32_e32 v16, v87, v53
	v_fmac_f32_e32 v17, v88, v53
	v_lshrrev_b32_e32 v84, 16, v79
	v_lshl_or_b32 v83, v84, 7, v89
	v_cmp_lt_i32_e32 vcc, 17, v78
	s_mov_b64 exec, vcc
	global_load_dwordx4 v[24:27], v83, s[12:13]
	s_mov_b64 exec, -1
	v_cvt_f32_f16_sdwa v53, v81 dst_sel:DWORD dst_unused:UNUSED_PAD src0_sel:WORD_1
	s_waitcnt lgkmcnt(0)
	ds_bpermute_b32 v79, v90, v74 offset:8
	ds_bpermute_b32 v81, v90, v76 offset:8
	s_waitcnt vmcnt(7)
	v_cvt_f32_ubyte0_e32 v85, v28
	v_cvt_f32_ubyte1_e32 v86, v28
	v_cvt_f32_ubyte2_e32 v87, v28
	v_cvt_f32_ubyte3_e32 v88, v28
	v_fmac_f32_e32 v2, v85, v54
	v_fmac_f32_e32 v3, v86, v54
	v_fmac_f32_e32 v4, v87, v54
	v_fmac_f32_e32 v5, v88, v54
	v_cvt_f32_ubyte0_e32 v85, v29
	v_cvt_f32_ubyte1_e32 v86, v29
	v_cvt_f32_ubyte2_e32 v87, v29
	v_cvt_f32_ubyte3_e32 v88, v29
	v_fmac_f32_e32 v6, v85, v54
	v_fmac_f32_e32 v7, v86, v54
	v_fmac_f32_e32 v8, v87, v54
	v_fmac_f32_e32 v9, v88, v54
	v_cvt_f32_ubyte0_e32 v85, v30
	v_cvt_f32_ubyte1_e32 v86, v30
	v_cvt_f32_ubyte2_e32 v87, v30
	v_cvt_f32_ubyte3_e32 v88, v30
	v_fmac_f32_e32 v10, v85, v54
	v_fmac_f32_e32 v11, v86, v54
	v_fmac_f32_e32 v12, v87, v54
	v_fmac_f32_e32 v13, v88, v54
	v_cvt_f32_ubyte0_e32 v85, v31
	v_cvt_f32_ubyte1_e32 v86, v31
	v_cvt_f32_ubyte2_e32 v87, v31
	v_cvt_f32_ubyte3_e32 v88, v31
	v_fmac_f32_e32 v14, v85, v54
	v_fmac_f32_e32 v15, v86, v54
	v_fmac_f32_e32 v16, v87, v54
	v_fmac_f32_e32 v17, v88, v54
	v_and_b32_e32 v84, 0xffff, v80
	v_lshl_or_b32 v83, v84, 7, v89
	v_cmp_lt_i32_e32 vcc, 18, v78
	s_mov_b64 exec, vcc
	global_load_dwordx4 v[28:31], v83, s[12:13]
	s_mov_b64 exec, -1
	v_cvt_f32_f16_e32 v54, v82
	s_waitcnt vmcnt(7)
	v_cvt_f32_ubyte0_e32 v85, v32
	v_cvt_f32_ubyte1_e32 v86, v32
	v_cvt_f32_ubyte2_e32 v87, v32
	v_cvt_f32_ubyte3_e32 v88, v32
	v_fmac_f32_e32 v2, v85, v55
	v_fmac_f32_e32 v3, v86, v55
	v_fmac_f32_e32 v4, v87, v55
	v_fmac_f32_e32 v5, v88, v55
	v_cvt_f32_ubyte0_e32 v85, v33
	v_cvt_f32_ubyte1_e32 v86, v33
	v_cvt_f32_ubyte2_e32 v87, v33
	v_cvt_f32_ubyte3_e32 v88, v33
	v_fmac_f32_e32 v6, v85, v55
	v_fmac_f32_e32 v7, v86, v55
	v_fmac_f32_e32 v8, v87, v55
	v_fmac_f32_e32 v9, v88, v55
	v_cvt_f32_ubyte0_e32 v85, v34
	v_cvt_f32_ubyte1_e32 v86, v34
	v_cvt_f32_ubyte2_e32 v87, v34
	v_cvt_f32_ubyte3_e32 v88, v34
	v_fmac_f32_e32 v10, v85, v55
	v_fmac_f32_e32 v11, v86, v55
	v_fmac_f32_e32 v12, v87, v55
	v_fmac_f32_e32 v13, v88, v55
	v_cvt_f32_ubyte0_e32 v85, v35
	v_cvt_f32_ubyte1_e32 v86, v35
	v_cvt_f32_ubyte2_e32 v87, v35
	v_cvt_f32_ubyte3_e32 v88, v35
	v_fmac_f32_e32 v14, v85, v55
	v_fmac_f32_e32 v15, v86, v55
	v_fmac_f32_e32 v16, v87, v55
	v_fmac_f32_e32 v17, v88, v55
	v_lshrrev_b32_e32 v84, 16, v80
	v_lshl_or_b32 v83, v84, 7, v89
	v_cmp_lt_i32_e32 vcc, 19, v78
	s_mov_b64 exec, vcc
	global_load_dwordx4 v[32:35], v83, s[12:13]
	s_mov_b64 exec, -1
	v_cvt_f32_f16_sdwa v55, v82 dst_sel:DWORD dst_unused:UNUSED_PAD src0_sel:WORD_1
	s_cmp_le_u32 s40, 20
	s_cbranch_scc1 .Lg2_tail4
	s_waitcnt lgkmcnt(0)
	ds_bpermute_b32 v80, v90, v74 offset:12
	ds_bpermute_b32 v82, v90, v76 offset:12
	s_waitcnt vmcnt(7)
	v_cvt_f32_ubyte0_e32 v85, v36
	v_cvt_f32_ubyte1_e32 v86, v36
	v_cvt_f32_ubyte2_e32 v87, v36
	v_cvt_f32_ubyte3_e32 v88, v36
	v_fmac_f32_e32 v2, v85, v56
	v_fmac_f32_e32 v3, v86, v56
	v_fmac_f32_e32 v4, v87, v56
	v_fmac_f32_e32 v5, v88, v56
	v_cvt_f32_ubyte0_e32 v85, v37
	v_cvt_f32_ubyte1_e32 v86, v37
	v_cvt_f32_ubyte2_e32 v87, v37
	v_cvt_f32_ubyte3_e32 v88, v37
	v_fmac_f32_e32 v6, v85, v56
	v_fmac_f32_e32 v7, v86, v56
	v_fmac_f32_e32 v8, v87, v56
	v_fmac_f32_e32 v9, v88, v56
	v_cvt_f32_ubyte0_e32 v85, v38
	v_cvt_f32_ubyte1_e32 v86, v38
	v_cvt_f32_ubyte2_e32 v87, v38
	v_cvt_f32_ubyte3_e32 v88, v38
	v_fmac_f32_e32 v10, v85, v56
	v_fmac_f32_e32 v11, v86, v56
	v_fmac_f32_e32 v12, v87, v56
	v_fmac_f32_e32 v13, v88, v56
	v_cvt_f32_ubyte0_e32 v85, v39
	v_cvt_f32_ubyte1_e32 v86, v39
	v_cvt_f32_ubyte2_e32 v87, v39
	v_cvt_f32_ubyte3_e32 v88, v39
	v_fmac_f32_e32 v14, v85, v56
	v_fmac_f32_e32 v15, v86, v56
	v_fmac_f32_e32 v16, v87, v56
	v_fmac_f32_e32 v17, v88, v56
	v_and_b32_e32 v84, 0xffff, v79
	v_lshl_or_b32 v83, v84, 7, v89
	v_cmp_lt_i32_e32 vcc, 20, v78
	s_mov_b64 exec, vcc
	global_load_dwordx4 v[36:39], v83, s[12:13]
	s_mov_b64 exec, -1
	v_cvt_f32_f16_e32 v56, v81
	s_waitcnt vmcnt(7)
	v_cvt_f32_ubyte0_e32 v85, v40
	v_cvt_f32_ubyte1_e32 v86, v40
	v_cvt_f32_ubyte2_e32 v87, v40
	v_cvt_f32_ubyte3_e32 v88, v40
	v_fmac_f32_e32 v2, v85, v57
	v_fmac_f32_e32 v3, v86, v57
	v_fmac_f32_e32 v4, v87, v57
	v_fmac_f32_e32 v5, v88, v57
	v_cvt_f32_ubyte0_e32 v85, v41
	v_cvt_f32_ubyte1_e32 v86, v41
	v_cvt_f32_ubyte2_e32 v87, v41
	v_cvt_f32_ubyte3_e32 v88, v41
	v_fmac_f32_e32 v6, v85, v57
	v_fmac_f32_e32 v7, v86, v57
	v_fmac_f32_e32 v8, v87, v57
	v_fmac_f32_e32 v9, v88, v57
	v_cvt_f32_ubyte0_e32 v85, v42
	v_cvt_f32_ubyte1_e32 v86, v42
	v_cvt_f32_ubyte2_e32 v87, v42
	v_cvt_f32_ubyte3_e32 v88, v42
	v_fmac_f32_e32 v10, v85, v57
	v_fmac_f32_e32 v11, v86, v57
	v_fmac_f32_e32 v12, v87, v57
	v_fmac_f32_e32 v13, v88, v57
	v_cvt_f32_ubyte0_e32 v85, v43
	v_cvt_f32_ubyte1_e32 v86, v43
	v_cvt_f32_ubyte2_e32 v87, v43
	v_cvt_f32_ubyte3_e32 v88, v43
	v_fmac_f32_e32 v14, v85, v57
	v_fmac_f32_e32 v15, v86, v57
	v_fmac_f32_e32 v16, v87, v57
	v_fmac_f32_e32 v17, v88, v57
	v_lshrrev_b32_e32 v84, 16, v79
	v_lshl_or_b32 v83, v84, 7, v89
	v_cmp_lt_i32_e32 vcc, 21, v78
	s_mov_b64 exec, vcc
	global_load_dwordx4 v[40:43], v83, s[12:13]
	s_mov_b64 exec, -1
	v_cvt_f32_f16_sdwa v57, v81 dst_sel:DWORD dst_unused:UNUSED_PAD src0_sel:WORD_1
	s_waitcnt lgkmcnt(0)
	ds_bpermute_b32 v79, v90, v74 offset:16
	ds_bpermute_b32 v81, v90, v76 offset:16
	s_waitcnt vmcnt(7)
	v_cvt_f32_ubyte0_e32 v85, v44
	v_cvt_f32_ubyte1_e32 v86, v44
	v_cvt_f32_ubyte2_e32 v87, v44
	v_cvt_f32_ubyte3_e32 v88, v44
	v_fmac_f32_e32 v2, v85, v58
	v_fmac_f32_e32 v3, v86, v58
	v_fmac_f32_e32 v4, v87, v58
	v_fmac_f32_e32 v5, v88, v58
	v_cvt_f32_ubyte0_e32 v85, v45
	v_cvt_f32_ubyte1_e32 v86, v45
	v_cvt_f32_ubyte2_e32 v87, v45
	v_cvt_f32_ubyte3_e32 v88, v45
	v_fmac_f32_e32 v6, v85, v58
	v_fmac_f32_e32 v7, v86, v58
	v_fmac_f32_e32 v8, v87, v58
	v_fmac_f32_e32 v9, v88, v58
	v_cvt_f32_ubyte0_e32 v85, v46
	v_cvt_f32_ubyte1_e32 v86, v46
	v_cvt_f32_ubyte2_e32 v87, v46
	v_cvt_f32_ubyte3_e32 v88, v46
	v_fmac_f32_e32 v10, v85, v58
	v_fmac_f32_e32 v11, v86, v58
	v_fmac_f32_e32 v12, v87, v58
	v_fmac_f32_e32 v13, v88, v58
	v_cvt_f32_ubyte0_e32 v85, v47
	v_cvt_f32_ubyte1_e32 v86, v47
	v_cvt_f32_ubyte2_e32 v87, v47
	v_cvt_f32_ubyte3_e32 v88, v47
	v_fmac_f32_e32 v14, v85, v58
	v_fmac_f32_e32 v15, v86, v58
	v_fmac_f32_e32 v16, v87, v58
	v_fmac_f32_e32 v17, v88, v58
	v_and_b32_e32 v84, 0xffff, v80
	v_lshl_or_b32 v83, v84, 7, v89
	v_cmp_lt_i32_e32 vcc, 22, v78
	s_mov_b64 exec, vcc
	global_load_dwordx4 v[44:47], v83, s[12:13]
	s_mov_b64 exec, -1
	v_cvt_f32_f16_e32 v58, v82
	s_waitcnt vmcnt(7)
	v_cvt_f32_ubyte0_e32 v85, v48
	v_cvt_f32_ubyte1_e32 v86, v48
	v_cvt_f32_ubyte2_e32 v87, v48
	v_cvt_f32_ubyte3_e32 v88, v48
	v_fmac_f32_e32 v2, v85, v59
	v_fmac_f32_e32 v3, v86, v59
	v_fmac_f32_e32 v4, v87, v59
	v_fmac_f32_e32 v5, v88, v59
	v_cvt_f32_ubyte0_e32 v85, v49
	v_cvt_f32_ubyte1_e32 v86, v49
	v_cvt_f32_ubyte2_e32 v87, v49
	v_cvt_f32_ubyte3_e32 v88, v49
	v_fmac_f32_e32 v6, v85, v59
	v_fmac_f32_e32 v7, v86, v59
	v_fmac_f32_e32 v8, v87, v59
	v_fmac_f32_e32 v9, v88, v59
	v_cvt_f32_ubyte0_e32 v85, v50
	v_cvt_f32_ubyte1_e32 v86, v50
	v_cvt_f32_ubyte2_e32 v87, v50
	v_cvt_f32_ubyte3_e32 v88, v50
	v_fmac_f32_e32 v10, v85, v59
	v_fmac_f32_e32 v11, v86, v59
	v_fmac_f32_e32 v12, v87, v59
	v_fmac_f32_e32 v13, v88, v59
	v_cvt_f32_ubyte0_e32 v85, v51
	v_cvt_f32_ubyte1_e32 v86, v51
	v_cvt_f32_ubyte2_e32 v87, v51
	v_cvt_f32_ubyte3_e32 v88, v51
	v_fmac_f32_e32 v14, v85, v59
	v_fmac_f32_e32 v15, v86, v59
	v_fmac_f32_e32 v16, v87, v59
	v_fmac_f32_e32 v17, v88, v59
	v_lshrrev_b32_e32 v84, 16, v80
	v_lshl_or_b32 v83, v84, 7, v89
	v_cmp_lt_i32_e32 vcc, 23, v78
	s_mov_b64 exec, vcc
	global_load_dwordx4 v[48:51], v83, s[12:13]
	s_mov_b64 exec, -1
	v_cvt_f32_f16_sdwa v59, v82 dst_sel:DWORD dst_unused:UNUSED_PAD src0_sel:WORD_1
	s_cmp_le_u32 s40, 24
	s_cbranch_scc1 .Lg2_tail0
	s_waitcnt lgkmcnt(0)
	ds_bpermute_b32 v80, v90, v74 offset:20
	ds_bpermute_b32 v82, v90, v76 offset:20
	s_waitcnt vmcnt(7)
	v_cvt_f32_ubyte0_e32 v85, v20
	v_cvt_f32_ubyte1_e32 v86, v20
	v_cvt_f32_ubyte2_e32 v87, v20
	v_cvt_f32_ubyte3_e32 v88, v20
	v_fmac_f32_e32 v2, v85, v52
	v_fmac_f32_e32 v3, v86, v52
	v_fmac_f32_e32 v4, v87, v52
	v_fmac_f32_e32 v5, v88, v52
	v_cvt_f32_ubyte0_e32 v85, v21
	v_cvt_f32_ubyte1_e32 v86, v21
	v_cvt_f32_ubyte2_e32 v87, v21
	v_cvt_f32_ubyte3_e32 v88, v21
	v_fmac_f32_e32 v6, v85, v52
	v_fmac_f32_e32 v7, v86, v52
	v_fmac_f32_e32 v8, v87, v52
	v_fmac_f32_e32 v9, v88, v52
	v_cvt_f32_ubyte0_e32 v85, v22
	v_cvt_f32_ubyte1_e32 v86, v22
	v_cvt_f32_ubyte2_e32 v87, v22
	v_cvt_f32_ubyte3_e32 v88, v22
	v_fmac_f32_e32 v10, v85, v52
	v_fmac_f32_e32 v11, v86, v52
	v_fmac_f32_e32 v12, v87, v52
	v_fmac_f32_e32 v13, v88, v52
	v_cvt_f32_ubyte0_e32 v85, v23
	v_cvt_f32_ubyte1_e32 v86, v23
	v_cvt_f32_ubyte2_e32 v87, v23
	v_cvt_f32_ubyte3_e32 v88, v23
	v_fmac_f32_e32 v14, v85, v52
	v_fmac_f32_e32 v15, v86, v52
	v_fmac_f32_e32 v16, v87, v52
	v_fmac_f32_e32 v17, v88, v52
	v_and_b32_e32 v84, 0xffff, v79
	v_lshl_or_b32 v83, v84, 7, v89
	v_cmp_lt_i32_e32 vcc, 24, v78
	s_mov_b64 exec, vcc
	global_load_dwordx4 v[20:23], v83, s[12:13]
	s_mov_b64 exec, -1
	v_cvt_f32_f16_e32 v52, v81
	s_waitcnt vmcnt(7)
	v_cvt_f32_ubyte0_e32 v85, v24
	v_cvt_f32_ubyte1_e32 v86, v24
	v_cvt_f32_ubyte2_e32 v87, v24
	v_cvt_f32_ubyte3_e32 v88, v24
	v_fmac_f32_e32 v2, v85, v53
	v_fmac_f32_e32 v3, v86, v53
	v_fmac_f32_e32 v4, v87, v53
	v_fmac_f32_e32 v5, v88, v53
	v_cvt_f32_ubyte0_e32 v85, v25
	v_cvt_f32_ubyte1_e32 v86, v25
	v_cvt_f32_ubyte2_e32 v87, v25
	v_cvt_f32_ubyte3_e32 v88, v25
	v_fmac_f32_e32 v6, v85, v53
	v_fmac_f32_e32 v7, v86, v53
	v_fmac_f32_e32 v8, v87, v53
	v_fmac_f32_e32 v9, v88, v53
	v_cvt_f32_ubyte0_e32 v85, v26
	v_cvt_f32_ubyte1_e32 v86, v26
	v_cvt_f32_ubyte2_e32 v87, v26
	v_cvt_f32_ubyte3_e32 v88, v26
	v_fmac_f32_e32 v10, v85, v53
	v_fmac_f32_e32 v11, v86, v53
	v_fmac_f32_e32 v12, v87, v53
	v_fmac_f32_e32 v13, v88, v53
	v_cvt_f32_ubyte0_e32 v85, v27
	v_cvt_f32_ubyte1_e32 v86, v27
	v_cvt_f32_ubyte2_e32 v87, v27
	v_cvt_f32_ubyte3_e32 v88, v27
	v_fmac_f32_e32 v14, v85, v53
	v_fmac_f32_e32 v15, v86, v53
	v_fmac_f32_e32 v16, v87, v53
	v_fmac_f32_e32 v17, v88, v53
	v_lshrrev_b32_e32 v84, 16, v79
	v_lshl_or_b32 v83, v84, 7, v89
	v_cmp_lt_i32_e32 vcc, 25, v78
	s_mov_b64 exec, vcc
	global_load_dwordx4 v[24:27], v83, s[12:13]
	s_mov_b64 exec, -1
	v_cvt_f32_f16_sdwa v53, v81 dst_sel:DWORD dst_unused:UNUSED_PAD src0_sel:WORD_1
	s_waitcnt lgkmcnt(0)
	ds_bpermute_b32 v79, v90, v74 offset:24
	ds_bpermute_b32 v81, v90, v76 offset:24
	s_waitcnt vmcnt(7)
	v_cvt_f32_ubyte0_e32 v85, v28
	v_cvt_f32_ubyte1_e32 v86, v28
	v_cvt_f32_ubyte2_e32 v87, v28
	v_cvt_f32_ubyte3_e32 v88, v28
	v_fmac_f32_e32 v2, v85, v54
	v_fmac_f32_e32 v3, v86, v54
	v_fmac_f32_e32 v4, v87, v54
	v_fmac_f32_e32 v5, v88, v54
	v_cvt_f32_ubyte0_e32 v85, v29
	v_cvt_f32_ubyte1_e32 v86, v29
	v_cvt_f32_ubyte2_e32 v87, v29
	v_cvt_f32_ubyte3_e32 v88, v29
	v_fmac_f32_e32 v6, v85, v54
	v_fmac_f32_e32 v7, v86, v54
	v_fmac_f32_e32 v8, v87, v54
	v_fmac_f32_e32 v9, v88, v54
	v_cvt_f32_ubyte0_e32 v85, v30
	v_cvt_f32_ubyte1_e32 v86, v30
	v_cvt_f32_ubyte2_e32 v87, v30
	v_cvt_f32_ubyte3_e32 v88, v30
	v_fmac_f32_e32 v10, v85, v54
	v_fmac_f32_e32 v11, v86, v54
	v_fmac_f32_e32 v12, v87, v54
	v_fmac_f32_e32 v13, v88, v54
	v_cvt_f32_ubyte0_e32 v85, v31
	v_cvt_f32_ubyte1_e32 v86, v31
	v_cvt_f32_ubyte2_e32 v87, v31
	v_cvt_f32_ubyte3_e32 v88, v31
	v_fmac_f32_e32 v14, v85, v54
	v_fmac_f32_e32 v15, v86, v54
	v_fmac_f32_e32 v16, v87, v54
	v_fmac_f32_e32 v17, v88, v54
	v_and_b32_e32 v84, 0xffff, v80
	v_lshl_or_b32 v83, v84, 7, v89
	v_cmp_lt_i32_e32 vcc, 26, v78
	s_mov_b64 exec, vcc
	global_load_dwordx4 v[28:31], v83, s[12:13]
	s_mov_b64 exec, -1
	v_cvt_f32_f16_e32 v54, v82
	s_waitcnt vmcnt(7)
	v_cvt_f32_ubyte0_e32 v85, v32
	v_cvt_f32_ubyte1_e32 v86, v32
	v_cvt_f32_ubyte2_e32 v87, v32
	v_cvt_f32_ubyte3_e32 v88, v32
	v_fmac_f32_e32 v2, v85, v55
	v_fmac_f32_e32 v3, v86, v55
	v_fmac_f32_e32 v4, v87, v55
	v_fmac_f32_e32 v5, v88, v55
	v_cvt_f32_ubyte0_e32 v85, v33
	v_cvt_f32_ubyte1_e32 v86, v33
	v_cvt_f32_ubyte2_e32 v87, v33
	v_cvt_f32_ubyte3_e32 v88, v33
	v_fmac_f32_e32 v6, v85, v55
	v_fmac_f32_e32 v7, v86, v55
	v_fmac_f32_e32 v8, v87, v55
	v_fmac_f32_e32 v9, v88, v55
	v_cvt_f32_ubyte0_e32 v85, v34
	v_cvt_f32_ubyte1_e32 v86, v34
	v_cvt_f32_ubyte2_e32 v87, v34
	v_cvt_f32_ubyte3_e32 v88, v34
	v_fmac_f32_e32 v10, v85, v55
	v_fmac_f32_e32 v11, v86, v55
	v_fmac_f32_e32 v12, v87, v55
	v_fmac_f32_e32 v13, v88, v55
	v_cvt_f32_ubyte0_e32 v85, v35
	v_cvt_f32_ubyte1_e32 v86, v35
	v_cvt_f32_ubyte2_e32 v87, v35
	v_cvt_f32_ubyte3_e32 v88, v35
	v_fmac_f32_e32 v14, v85, v55
	v_fmac_f32_e32 v15, v86, v55
	v_fmac_f32_e32 v16, v87, v55
	v_fmac_f32_e32 v17, v88, v55
	v_lshrrev_b32_e32 v84, 16, v80
	v_lshl_or_b32 v83, v84, 7, v89
	v_cmp_lt_i32_e32 vcc, 27, v78
	s_mov_b64 exec, vcc
	global_load_dwordx4 v[32:35], v83, s[12:13]
	s_mov_b64 exec, -1
	v_cvt_f32_f16_sdwa v55, v82 dst_sel:DWORD dst_unused:UNUSED_PAD src0_sel:WORD_1
	s_cmp_le_u32 s40, 28
	s_cbranch_scc1 .Lg2_tail4
	s_waitcnt lgkmcnt(0)
	ds_bpermute_b32 v80, v90, v74 offset:28
	ds_bpermute_b32 v82, v90, v76 offset:28
	s_waitcnt vmcnt(7)
	v_cvt_f32_ubyte0_e32 v85, v36
	v_cvt_f32_ubyte1_e32 v86, v36
	v_cvt_f32_ubyte2_e32 v87, v36
	v_cvt_f32_ubyte3_e32 v88, v36
	v_fmac_f32_e32 v2, v85, v56
	v_fmac_f32_e32 v3, v86, v56
	v_fmac_f32_e32 v4, v87, v56
	v_fmac_f32_e32 v5, v88, v56
	v_cvt_f32_ubyte0_e32 v85, v37
	v_cvt_f32_ubyte1_e32 v86, v37
	v_cvt_f32_ubyte2_e32 v87, v37
	v_cvt_f32_ubyte3_e32 v88, v37
	v_fmac_f32_e32 v6, v85, v56
	v_fmac_f32_e32 v7, v86, v56
	v_fmac_f32_e32 v8, v87, v56
	v_fmac_f32_e32 v9, v88, v56
	v_cvt_f32_ubyte0_e32 v85, v38
	v_cvt_f32_ubyte1_e32 v86, v38
	v_cvt_f32_ubyte2_e32 v87, v38
	v_cvt_f32_ubyte3_e32 v88, v38
	v_fmac_f32_e32 v10, v85, v56
	v_fmac_f32_e32 v11, v86, v56
	v_fmac_f32_e32 v12, v87, v56
	v_fmac_f32_e32 v13, v88, v56
	v_cvt_f32_ubyte0_e32 v85, v39
	v_cvt_f32_ubyte1_e32 v86, v39
	v_cvt_f32_ubyte2_e32 v87, v39
	v_cvt_f32_ubyte3_e32 v88, v39
	v_fmac_f32_e32 v14, v85, v56
	v_fmac_f32_e32 v15, v86, v56
	v_fmac_f32_e32 v16, v87, v56
	v_fmac_f32_e32 v17, v88, v56
	v_and_b32_e32 v84, 0xffff, v79
	v_lshl_or_b32 v83, v84, 7, v89
	v_cmp_lt_i32_e32 vcc, 28, v78
	s_mov_b64 exec, vcc
	global_load_dwordx4 v[36:39], v83, s[12:13]
	s_mov_b64 exec, -1
	v_cvt_f32_f16_e32 v56, v81
	s_waitcnt vmcnt(7)
	v_cvt_f32_ubyte0_e32 v85, v40
	v_cvt_f32_ubyte1_e32 v86, v40
	v_cvt_f32_ubyte2_e32 v87, v40
	v_cvt_f32_ubyte3_e32 v88, v40
	v_fmac_f32_e32 v2, v85, v57
	v_fmac_f32_e32 v3, v86, v57
	v_fmac_f32_e32 v4, v87, v57
	v_fmac_f32_e32 v5, v88, v57
	v_cvt_f32_ubyte0_e32 v85, v41
	v_cvt_f32_ubyte1_e32 v86, v41
	v_cvt_f32_ubyte2_e32 v87, v41
	v_cvt_f32_ubyte3_e32 v88, v41
	v_fmac_f32_e32 v6, v85, v57
	v_fmac_f32_e32 v7, v86, v57
	v_fmac_f32_e32 v8, v87, v57
	v_fmac_f32_e32 v9, v88, v57
	v_cvt_f32_ubyte0_e32 v85, v42
	v_cvt_f32_ubyte1_e32 v86, v42
	v_cvt_f32_ubyte2_e32 v87, v42
	v_cvt_f32_ubyte3_e32 v88, v42
	v_fmac_f32_e32 v10, v85, v57
	v_fmac_f32_e32 v11, v86, v57
	v_fmac_f32_e32 v12, v87, v57
	v_fmac_f32_e32 v13, v88, v57
	v_cvt_f32_ubyte0_e32 v85, v43
	v_cvt_f32_ubyte1_e32 v86, v43
	v_cvt_f32_ubyte2_e32 v87, v43
	v_cvt_f32_ubyte3_e32 v88, v43
	v_fmac_f32_e32 v14, v85, v57
	v_fmac_f32_e32 v15, v86, v57
	v_fmac_f32_e32 v16, v87, v57
	v_fmac_f32_e32 v17, v88, v57
	v_lshrrev_b32_e32 v84, 16, v79
	v_lshl_or_b32 v83, v84, 7, v89
	v_cmp_lt_i32_e32 vcc, 29, v78
	s_mov_b64 exec, vcc
	global_load_dwordx4 v[40:43], v83, s[12:13]
	s_mov_b64 exec, -1
	v_cvt_f32_f16_sdwa v57, v81 dst_sel:DWORD dst_unused:UNUSED_PAD src0_sel:WORD_1
	s_waitcnt lgkmcnt(0)
	s_waitcnt vmcnt(7)
	v_cvt_f32_ubyte0_e32 v85, v44
	v_cvt_f32_ubyte1_e32 v86, v44
	v_cvt_f32_ubyte2_e32 v87, v44
	v_cvt_f32_ubyte3_e32 v88, v44
	v_fmac_f32_e32 v2, v85, v58
	v_fmac_f32_e32 v3, v86, v58
	v_fmac_f32_e32 v4, v87, v58
	v_fmac_f32_e32 v5, v88, v58
	v_cvt_f32_ubyte0_e32 v85, v45
	v_cvt_f32_ubyte1_e32 v86, v45
	v_cvt_f32_ubyte2_e32 v87, v45
	v_cvt_f32_ubyte3_e32 v88, v45
	v_fmac_f32_e32 v6, v85, v58
	v_fmac_f32_e32 v7, v86, v58
	v_fmac_f32_e32 v8, v87, v58
	v_fmac_f32_e32 v9, v88, v58
	v_cvt_f32_ubyte0_e32 v85, v46
	v_cvt_f32_ubyte1_e32 v86, v46
	v_cvt_f32_ubyte2_e32 v87, v46
	v_cvt_f32_ubyte3_e32 v88, v46
	v_fmac_f32_e32 v10, v85, v58
	v_fmac_f32_e32 v11, v86, v58
	v_fmac_f32_e32 v12, v87, v58
	v_fmac_f32_e32 v13, v88, v58
	v_cvt_f32_ubyte0_e32 v85, v47
	v_cvt_f32_ubyte1_e32 v86, v47
	v_cvt_f32_ubyte2_e32 v87, v47
	v_cvt_f32_ubyte3_e32 v88, v47
	v_fmac_f32_e32 v14, v85, v58
	v_fmac_f32_e32 v15, v86, v58
	v_fmac_f32_e32 v16, v87, v58
	v_fmac_f32_e32 v17, v88, v58
	v_and_b32_e32 v84, 0xffff, v80
	v_lshl_or_b32 v83, v84, 7, v89
	v_cmp_lt_i32_e32 vcc, 30, v78
	s_mov_b64 exec, vcc
	global_load_dwordx4 v[44:47], v83, s[12:13]
	s_mov_b64 exec, -1
	v_cvt_f32_f16_e32 v58, v82
	s_waitcnt vmcnt(7)
	v_cvt_f32_ubyte0_e32 v85, v48
	v_cvt_f32_ubyte1_e32 v86, v48
	v_cvt_f32_ubyte2_e32 v87, v48
	v_cvt_f32_ubyte3_e32 v88, v48
	v_fmac_f32_e32 v2, v85, v59
	v_fmac_f32_e32 v3, v86, v59
	v_fmac_f32_e32 v4, v87, v59
	v_fmac_f32_e32 v5, v88, v59
	v_cvt_f32_ubyte0_e32 v85, v49
	v_cvt_f32_ubyte1_e32 v86, v49
	v_cvt_f32_ubyte2_e32 v87, v49
	v_cvt_f32_ubyte3_e32 v88, v49
	v_fmac_f32_e32 v6, v85, v59
	v_fmac_f32_e32 v7, v86, v59
	v_fmac_f32_e32 v8, v87, v59
	v_fmac_f32_e32 v9, v88, v59
	v_cvt_f32_ubyte0_e32 v85, v50
	v_cvt_f32_ubyte1_e32 v86, v50
	v_cvt_f32_ubyte2_e32 v87, v50
	v_cvt_f32_ubyte3_e32 v88, v50
	v_fmac_f32_e32 v10, v85, v59
	v_fmac_f32_e32 v11, v86, v59
	v_fmac_f32_e32 v12, v87, v59
	v_fmac_f32_e32 v13, v88, v59
	v_cvt_f32_ubyte0_e32 v85, v51
	v_cvt_f32_ubyte1_e32 v86, v51
	v_cvt_f32_ubyte2_e32 v87, v51
	v_cvt_f32_ubyte3_e32 v88, v51
	v_fmac_f32_e32 v14, v85, v59
	v_fmac_f32_e32 v15, v86, v59
	v_fmac_f32_e32 v16, v87, v59
	v_fmac_f32_e32 v17, v88, v59
	v_lshrrev_b32_e32 v84, 16, v80
	v_lshl_or_b32 v83, v84, 7, v89
	v_cmp_lt_i32_e32 vcc, 31, v78
	s_mov_b64 exec, vcc
	global_load_dwordx4 v[48:51], v83, s[12:13]
	s_mov_b64 exec, -1
	v_cvt_f32_f16_sdwa v59, v82 dst_sel:DWORD dst_unused:UNUSED_PAD src0_sel:WORD_1
.Lg2_tail0:
	s_waitcnt vmcnt(7)
	v_cvt_f32_ubyte0_e32 v85, v20
	v_cvt_f32_ubyte1_e32 v86, v20
	v_cvt_f32_ubyte2_e32 v87, v20
	v_cvt_f32_ubyte3_e32 v88, v20
	v_fmac_f32_e32 v2, v85, v52
	v_fmac_f32_e32 v3, v86, v52
	v_fmac_f32_e32 v4, v87, v52
	v_fmac_f32_e32 v5, v88, v52
	v_cvt_f32_ubyte0_e32 v85, v21
	v_cvt_f32_ubyte1_e32 v86, v21
	v_cvt_f32_ubyte2_e32 v87, v21
	v_cvt_f32_ubyte3_e32 v88, v21
	v_fmac_f32_e32 v6, v85, v52
	v_fmac_f32_e32 v7, v86, v52
	v_fmac_f32_e32 v8, v87, v52
	v_fmac_f32_e32 v9, v88, v52
	v_cvt_f32_ubyte0_e32 v85, v22
	v_cvt_f32_ubyte1_e32 v86, v22
	v_cvt_f32_ubyte2_e32 v87, v22
	v_cvt_f32_ubyte3_e32 v88, v22
	v_fmac_f32_e32 v10, v85, v52
	v_fmac_f32_e32 v11, v86, v52
	v_fmac_f32_e32 v12, v87, v52
	v_fmac_f32_e32 v13, v88, v52
	v_cvt_f32_ubyte0_e32 v85, v23
	v_cvt_f32_ubyte1_e32 v86, v23
	v_cvt_f32_ubyte2_e32 v87, v23
	v_cvt_f32_ubyte3_e32 v88, v23
	v_fmac_f32_e32 v14, v85, v52
	v_fmac_f32_e32 v15, v86, v52
	v_fmac_f32_e32 v16, v87, v52
	v_fmac_f32_e32 v17, v88, v52
	s_waitcnt vmcnt(6)
	v_cvt_f32_ubyte0_e32 v85, v24
	v_cvt_f32_ubyte1_e32 v86, v24
	v_cvt_f32_ubyte2_e32 v87, v24
	v_cvt_f32_ubyte3_e32 v88, v24
	v_fmac_f32_e32 v2, v85, v53
	v_fmac_f32_e32 v3, v86, v53
	v_fmac_f32_e32 v4, v87, v53
	v_fmac_f32_e32 v5, v88, v53
	v_cvt_f32_ubyte0_e32 v85, v25
	v_cvt_f32_ubyte1_e32 v86, v25
	v_cvt_f32_ubyte2_e32 v87, v25
	v_cvt_f32_ubyte3_e32 v88, v25
	v_fmac_f32_e32 v6, v85, v53
	v_fmac_f32_e32 v7, v86, v53
	v_fmac_f32_e32 v8, v87, v53
	v_fmac_f32_e32 v9, v88, v53
	v_cvt_f32_ubyte0_e32 v85, v26
	v_cvt_f32_ubyte1_e32 v86, v26
	v_cvt_f32_ubyte2_e32 v87, v26
	v_cvt_f32_ubyte3_e32 v88, v26
	v_fmac_f32_e32 v10, v85, v53
	v_fmac_f32_e32 v11, v86, v53
	v_fmac_f32_e32 v12, v87, v53
	v_fmac_f32_e32 v13, v88, v53
	v_cvt_f32_ubyte0_e32 v85, v27
	v_cvt_f32_ubyte1_e32 v86, v27
	v_cvt_f32_ubyte2_e32 v87, v27
	v_cvt_f32_ubyte3_e32 v88, v27
	v_fmac_f32_e32 v14, v85, v53
	v_fmac_f32_e32 v15, v86, v53
	v_fmac_f32_e32 v16, v87, v53
	v_fmac_f32_e32 v17, v88, v53
	s_waitcnt vmcnt(5)
	v_cvt_f32_ubyte0_e32 v85, v28
	v_cvt_f32_ubyte1_e32 v86, v28
	v_cvt_f32_ubyte2_e32 v87, v28
	v_cvt_f32_ubyte3_e32 v88, v28
	v_fmac_f32_e32 v2, v85, v54
	v_fmac_f32_e32 v3, v86, v54
	v_fmac_f32_e32 v4, v87, v54
	v_fmac_f32_e32 v5, v88, v54
	v_cvt_f32_ubyte0_e32 v85, v29
	v_cvt_f32_ubyte1_e32 v86, v29
	v_cvt_f32_ubyte2_e32 v87, v29
	v_cvt_f32_ubyte3_e32 v88, v29
	v_fmac_f32_e32 v6, v85, v54
	v_fmac_f32_e32 v7, v86, v54
	v_fmac_f32_e32 v8, v87, v54
	v_fmac_f32_e32 v9, v88, v54
	v_cvt_f32_ubyte0_e32 v85, v30
	v_cvt_f32_ubyte1_e32 v86, v30
	v_cvt_f32_ubyte2_e32 v87, v30
	v_cvt_f32_ubyte3_e32 v88, v30
	v_fmac_f32_e32 v10, v85, v54
	v_fmac_f32_e32 v11, v86, v54
	v_fmac_f32_e32 v12, v87, v54
	v_fmac_f32_e32 v13, v88, v54
	v_cvt_f32_ubyte0_e32 v85, v31
	v_cvt_f32_ubyte1_e32 v86, v31
	v_cvt_f32_ubyte2_e32 v87, v31
	v_cvt_f32_ubyte3_e32 v88, v31
	v_fmac_f32_e32 v14, v85, v54
	v_fmac_f32_e32 v15, v86, v54
	v_fmac_f32_e32 v16, v87, v54
	v_fmac_f32_e32 v17, v88, v54
	s_waitcnt vmcnt(4)
	v_cvt_f32_ubyte0_e32 v85, v32
	v_cvt_f32_ubyte1_e32 v86, v32
	v_cvt_f32_ubyte2_e32 v87, v32
	v_cvt_f32_ubyte3_e32 v88, v32
	v_fmac_f32_e32 v2, v85, v55
	v_fmac_f32_e32 v3, v86, v55
	v_fmac_f32_e32 v4, v87, v55
	v_fmac_f32_e32 v5, v88, v55
	v_cvt_f32_ubyte0_e32 v85, v33
	v_cvt_f32_ubyte1_e32 v86, v33
	v_cvt_f32_ubyte2_e32 v87, v33
	v_cvt_f32_ubyte3_e32 v88, v33
	v_fmac_f32_e32 v6, v85, v55
	v_fmac_f32_e32 v7, v86, v55
	v_fmac_f32_e32 v8, v87, v55
	v_fmac_f32_e32 v9, v88, v55
	v_cvt_f32_ubyte0_e32 v85, v34
	v_cvt_f32_ubyte1_e32 v86, v34
	v_cvt_f32_ubyte2_e32 v87, v34
	v_cvt_f32_ubyte3_e32 v88, v34
	v_fmac_f32_e32 v10, v85, v55
	v_fmac_f32_e32 v11, v86, v55
	v_fmac_f32_e32 v12, v87, v55
	v_fmac_f32_e32 v13, v88, v55
	v_cvt_f32_ubyte0_e32 v85, v35
	v_cvt_f32_ubyte1_e32 v86, v35
	v_cvt_f32_ubyte2_e32 v87, v35
	v_cvt_f32_ubyte3_e32 v88, v35
	v_fmac_f32_e32 v14, v85, v55
	v_fmac_f32_e32 v15, v86, v55
	v_fmac_f32_e32 v16, v87, v55
	v_fmac_f32_e32 v17, v88, v55
	s_waitcnt vmcnt(3)
	v_cvt_f32_ubyte0_e32 v85, v36
	v_cvt_f32_ubyte1_e32 v86, v36
	v_cvt_f32_ubyte2_e32 v87, v36
	v_cvt_f32_ubyte3_e32 v88, v36
	v_fmac_f32_e32 v2, v85, v56
	v_fmac_f32_e32 v3, v86, v56
	v_fmac_f32_e32 v4, v87, v56
	v_fmac_f32_e32 v5, v88, v56
	v_cvt_f32_ubyte0_e32 v85, v37
	v_cvt_f32_ubyte1_e32 v86, v37
	v_cvt_f32_ubyte2_e32 v87, v37
	v_cvt_f32_ubyte3_e32 v88, v37
	v_fmac_f32_e32 v6, v85, v56
	v_fmac_f32_e32 v7, v86, v56
	v_fmac_f32_e32 v8, v87, v56
	v_fmac_f32_e32 v9, v88, v56
	v_cvt_f32_ubyte0_e32 v85, v38
	v_cvt_f32_ubyte1_e32 v86, v38
	v_cvt_f32_ubyte2_e32 v87, v38
	v_cvt_f32_ubyte3_e32 v88, v38
	v_fmac_f32_e32 v10, v85, v56
	v_fmac_f32_e32 v11, v86, v56
	v_fmac_f32_e32 v12, v87, v56
	v_fmac_f32_e32 v13, v88, v56
	v_cvt_f32_ubyte0_e32 v85, v39
	v_cvt_f32_ubyte1_e32 v86, v39
	v_cvt_f32_ubyte2_e32 v87, v39
	v_cvt_f32_ubyte3_e32 v88, v39
	v_fmac_f32_e32 v14, v85, v56
	v_fmac_f32_e32 v15, v86, v56
	v_fmac_f32_e32 v16, v87, v56
	v_fmac_f32_e32 v17, v88, v56
	s_waitcnt vmcnt(2)
	v_cvt_f32_ubyte0_e32 v85, v40
	v_cvt_f32_ubyte1_e32 v86, v40
	v_cvt_f32_ubyte2_e32 v87, v40
	v_cvt_f32_ubyte3_e32 v88, v40
	v_fmac_f32_e32 v2, v85, v57
	v_fmac_f32_e32 v3, v86, v57
	v_fmac_f32_e32 v4, v87, v57
	v_fmac_f32_e32 v5, v88, v57
	v_cvt_f32_ubyte0_e32 v85, v41
	v_cvt_f32_ubyte1_e32 v86, v41
	v_cvt_f32_ubyte2_e32 v87, v41
	v_cvt_f32_ubyte3_e32 v88, v41
	v_fmac_f32_e32 v6, v85, v57
	v_fmac_f32_e32 v7, v86, v57
	v_fmac_f32_e32 v8, v87, v57
	v_fmac_f32_e32 v9, v88, v57
	v_cvt_f32_ubyte0_e32 v85, v42
	v_cvt_f32_ubyte1_e32 v86, v42
	v_cvt_f32_ubyte2_e32 v87, v42
	v_cvt_f32_ubyte3_e32 v88, v42
	v_fmac_f32_e32 v10, v85, v57
	v_fmac_f32_e32 v11, v86, v57
	v_fmac_f32_e32 v12, v87, v57
	v_fmac_f32_e32 v13, v88, v57
	v_cvt_f32_ubyte0_e32 v85, v43
	v_cvt_f32_ubyte1_e32 v86, v43
	v_cvt_f32_ubyte2_e32 v87, v43
	v_cvt_f32_ubyte3_e32 v88, v43
	v_fmac_f32_e32 v14, v85, v57
	v_fmac_f32_e32 v15, v86, v57
	v_fmac_f32_e32 v16, v87, v57
	v_fmac_f32_e32 v17, v88, v57
	s_waitcnt vmcnt(1)
	v_cvt_f32_ubyte0_e32 v85, v44
	v_cvt_f32_ubyte1_e32 v86, v44
	v_cvt_f32_ubyte2_e32 v87, v44
	v_cvt_f32_ubyte3_e32 v88, v44
	v_fmac_f32_e32 v2, v85, v58
	v_fmac_f32_e32 v3, v86, v58
	v_fmac_f32_e32 v4, v87, v58
	v_fmac_f32_e32 v5, v88, v58
	v_cvt_f32_ubyte0_e32 v85, v45
	v_cvt_f32_ubyte1_e32 v86, v45
	v_cvt_f32_ubyte2_e32 v87, v45
	v_cvt_f32_ubyte3_e32 v88, v45
	v_fmac_f32_e32 v6, v85, v58
	v_fmac_f32_e32 v7, v86, v58
	v_fmac_f32_e32 v8, v87, v58
	v_fmac_f32_e32 v9, v88, v58
	v_cvt_f32_ubyte0_e32 v85, v46
	v_cvt_f32_ubyte1_e32 v86, v46
	v_cvt_f32_ubyte2_e32 v87, v46
	v_cvt_f32_ubyte3_e32 v88, v46
	v_fmac_f32_e32 v10, v85, v58
	v_fmac_f32_e32 v11, v86, v58
	v_fmac_f32_e32 v12, v87, v58
	v_fmac_f32_e32 v13, v88, v58
	v_cvt_f32_ubyte0_e32 v85, v47
	v_cvt_f32_ubyte1_e32 v86, v47
	v_cvt_f32_ubyte2_e32 v87, v47
	v_cvt_f32_ubyte3_e32 v88, v47
	v_fmac_f32_e32 v14, v85, v58
	v_fmac_f32_e32 v15, v86, v58
	v_fmac_f32_e32 v16, v87, v58
	v_fmac_f32_e32 v17, v88, v58
	s_waitcnt vmcnt(0)
	v_cvt_f32_ubyte0_e32 v85, v48
	v_cvt_f32_ubyte1_e32 v86, v48
	v_cvt_f32_ubyte2_e32 v87, v48
	v_cvt_f32_ubyte3_e32 v88, v48
	v_fmac_f32_e32 v2, v85, v59
	v_fmac_f32_e32 v3, v86, v59
	v_fmac_f32_e32 v4, v87, v59
	v_fmac_f32_e32 v5, v88, v59
	v_cvt_f32_ubyte0_e32 v85, v49
	v_cvt_f32_ubyte1_e32 v86, v49
	v_cvt_f32_ubyte2_e32 v87, v49
	v_cvt_f32_ubyte3_e32 v88, v49
	v_fmac_f32_e32 v6, v85, v59
	v_fmac_f32_e32 v7, v86, v59
	v_fmac_f32_e32 v8, v87, v59
	v_fmac_f32_e32 v9, v88, v59
	v_cvt_f32_ubyte0_e32 v85, v50
	v_cvt_f32_ubyte1_e32 v86, v50
	v_cvt_f32_ubyte2_e32 v87, v50
	v_cvt_f32_ubyte3_e32 v88, v50
	v_fmac_f32_e32 v10, v85, v59
	v_fmac_f32_e32 v11, v86, v59
	v_fmac_f32_e32 v12, v87, v59
	v_fmac_f32_e32 v13, v88, v59
	v_cvt_f32_ubyte0_e32 v85, v51
	v_cvt_f32_ubyte1_e32 v86, v51
	v_cvt_f32_ubyte2_e32 v87, v51
	v_cvt_f32_ubyte3_e32 v88, v51
	v_fmac_f32_e32 v14, v85, v59
	v_fmac_f32_e32 v15, v86, v59
	v_fmac_f32_e32 v16, v87, v59
	v_fmac_f32_e32 v17, v88, v59
	s_branch .Lg2_rare_check
.Lg2_tail4:
	s_waitcnt vmcnt(7)
	v_cvt_f32_ubyte0_e32 v85, v36
	v_cvt_f32_ubyte1_e32 v86, v36
	v_cvt_f32_ubyte2_e32 v87, v36
	v_cvt_f32_ubyte3_e32 v88, v36
	v_fmac_f32_e32 v2, v85, v56
	v_fmac_f32_e32 v3, v86, v56
	v_fmac_f32_e32 v4, v87, v56
	v_fmac_f32_e32 v5, v88, v56
	v_cvt_f32_ubyte0_e32 v85, v37
	v_cvt_f32_ubyte1_e32 v86, v37
	v_cvt_f32_ubyte2_e32 v87, v37
	v_cvt_f32_ubyte3_e32 v88, v37
	v_fmac_f32_e32 v6, v85, v56
	v_fmac_f32_e32 v7, v86, v56
	v_fmac_f32_e32 v8, v87, v56
	v_fmac_f32_e32 v9, v88, v56
	v_cvt_f32_ubyte0_e32 v85, v38
	v_cvt_f32_ubyte1_e32 v86, v38
	v_cvt_f32_ubyte2_e32 v87, v38
	v_cvt_f32_ubyte3_e32 v88, v38
	v_fmac_f32_e32 v10, v85, v56
	v_fmac_f32_e32 v11, v86, v56
	v_fmac_f32_e32 v12, v87, v56
	v_fmac_f32_e32 v13, v88, v56
	v_cvt_f32_ubyte0_e32 v85, v39
	v_cvt_f32_ubyte1_e32 v86, v39
	v_cvt_f32_ubyte2_e32 v87, v39
	v_cvt_f32_ubyte3_e32 v88, v39
	v_fmac_f32_e32 v14, v85, v56
	v_fmac_f32_e32 v15, v86, v56
	v_fmac_f32_e32 v16, v87, v56
	v_fmac_f32_e32 v17, v88, v56
	s_waitcnt vmcnt(6)
	v_cvt_f32_ubyte0_e32 v85, v40
	v_cvt_f32_ubyte1_e32 v86, v40
	v_cvt_f32_ubyte2_e32 v87, v40
	v_cvt_f32_ubyte3_e32 v88, v40
	v_fmac_f32_e32 v2, v85, v57
	v_fmac_f32_e32 v3, v86, v57
	v_fmac_f32_e32 v4, v87, v57
	v_fmac_f32_e32 v5, v88, v57
	v_cvt_f32_ubyte0_e32 v85, v41
	v_cvt_f32_ubyte1_e32 v86, v41
	v_cvt_f32_ubyte2_e32 v87, v41
	v_cvt_f32_ubyte3_e32 v88, v41
	v_fmac_f32_e32 v6, v85, v57
	v_fmac_f32_e32 v7, v86, v57
	v_fmac_f32_e32 v8, v87, v57
	v_fmac_f32_e32 v9, v88, v57
	v_cvt_f32_ubyte0_e32 v85, v42
	v_cvt_f32_ubyte1_e32 v86, v42
	v_cvt_f32_ubyte2_e32 v87, v42
	v_cvt_f32_ubyte3_e32 v88, v42
	v_fmac_f32_e32 v10, v85, v57
	v_fmac_f32_e32 v11, v86, v57
	v_fmac_f32_e32 v12, v87, v57
	v_fmac_f32_e32 v13, v88, v57
	v_cvt_f32_ubyte0_e32 v85, v43
	v_cvt_f32_ubyte1_e32 v86, v43
	v_cvt_f32_ubyte2_e32 v87, v43
	v_cvt_f32_ubyte3_e32 v88, v43
	v_fmac_f32_e32 v14, v85, v57
	v_fmac_f32_e32 v15, v86, v57
	v_fmac_f32_e32 v16, v87, v57
	v_fmac_f32_e32 v17, v88, v57
	s_waitcnt vmcnt(5)
	v_cvt_f32_ubyte0_e32 v85, v44
	v_cvt_f32_ubyte1_e32 v86, v44
	v_cvt_f32_ubyte2_e32 v87, v44
	v_cvt_f32_ubyte3_e32 v88, v44
	v_fmac_f32_e32 v2, v85, v58
	v_fmac_f32_e32 v3, v86, v58
	v_fmac_f32_e32 v4, v87, v58
	v_fmac_f32_e32 v5, v88, v58
	v_cvt_f32_ubyte0_e32 v85, v45
	v_cvt_f32_ubyte1_e32 v86, v45
	v_cvt_f32_ubyte2_e32 v87, v45
	v_cvt_f32_ubyte3_e32 v88, v45
	v_fmac_f32_e32 v6, v85, v58
	v_fmac_f32_e32 v7, v86, v58
	v_fmac_f32_e32 v8, v87, v58
	v_fmac_f32_e32 v9, v88, v58
	v_cvt_f32_ubyte0_e32 v85, v46
	v_cvt_f32_ubyte1_e32 v86, v46
	v_cvt_f32_ubyte2_e32 v87, v46
	v_cvt_f32_ubyte3_e32 v88, v46
	v_fmac_f32_e32 v10, v85, v58
	v_fmac_f32_e32 v11, v86, v58
	v_fmac_f32_e32 v12, v87, v58
	v_fmac_f32_e32 v13, v88, v58
	v_cvt_f32_ubyte0_e32 v85, v47
	v_cvt_f32_ubyte1_e32 v86, v47
	v_cvt_f32_ubyte2_e32 v87, v47
	v_cvt_f32_ubyte3_e32 v88, v47
	v_fmac_f32_e32 v14, v85, v58
	v_fmac_f32_e32 v15, v86, v58
	v_fmac_f32_e32 v16, v87, v58
	v_fmac_f32_e32 v17, v88, v58
	s_waitcnt vmcnt(4)
	v_cvt_f32_ubyte0_e32 v85, v48
	v_cvt_f32_ubyte1_e32 v86, v48
	v_cvt_f32_ubyte2_e32 v87, v48
	v_cvt_f32_ubyte3_e32 v88, v48
	v_fmac_f32_e32 v2, v85, v59
	v_fmac_f32_e32 v3, v86, v59
	v_fmac_f32_e32 v4, v87, v59
	v_fmac_f32_e32 v5, v88, v59
	v_cvt_f32_ubyte0_e32 v85, v49
	v_cvt_f32_ubyte1_e32 v86, v49
	v_cvt_f32_ubyte2_e32 v87, v49
	v_cvt_f32_ubyte3_e32 v88, v49
	v_fmac_f32_e32 v6, v85, v59
	v_fmac_f32_e32 v7, v86, v59
	v_fmac_f32_e32 v8, v87, v59
	v_fmac_f32_e32 v9, v88, v59
	v_cvt_f32_ubyte0_e32 v85, v50
	v_cvt_f32_ubyte1_e32 v86, v50
	v_cvt_f32_ubyte2_e32 v87, v50
	v_cvt_f32_ubyte3_e32 v88, v50
	v_fmac_f32_e32 v10, v85, v59
	v_fmac_f32_e32 v11, v86, v59
	v_fmac_f32_e32 v12, v87, v59
	v_fmac_f32_e32 v13, v88, v59
	v_cvt_f32_ubyte0_e32 v85, v51
	v_cvt_f32_ubyte1_e32 v86, v51
	v_cvt_f32_ubyte2_e32 v87, v51
	v_cvt_f32_ubyte3_e32 v88, v51
	v_fmac_f32_e32 v14, v85, v59
	v_fmac_f32_e32 v15, v86, v59
	v_fmac_f32_e32 v16, v87, v59
	v_fmac_f32_e32 v17, v88, v59
	s_waitcnt vmcnt(3)
	v_cvt_f32_ubyte0_e32 v85, v20
	v_cvt_f32_ubyte1_e32 v86, v20
	v_cvt_f32_ubyte2_e32 v87, v20
	v_cvt_f32_ubyte3_e32 v88, v20
	v_fmac_f32_e32 v2, v85, v52
	v_fmac_f32_e32 v3, v86, v52
	v_fmac_f32_e32 v4, v87, v52
	v_fmac_f32_e32 v5, v88, v52
	v_cvt_f32_ubyte0_e32 v85, v21
	v_cvt_f32_ubyte1_e32 v86, v21
	v_cvt_f32_ubyte2_e32 v87, v21
	v_cvt_f32_ubyte3_e32 v88, v21
	v_fmac_f32_e32 v6, v85, v52
	v_fmac_f32_e32 v7, v86, v52
	v_fmac_f32_e32 v8, v87, v52
	v_fmac_f32_e32 v9, v88, v52
	v_cvt_f32_ubyte0_e32 v85, v22
	v_cvt_f32_ubyte1_e32 v86, v22
	v_cvt_f32_ubyte2_e32 v87, v22
	v_cvt_f32_ubyte3_e32 v88, v22
	v_fmac_f32_e32 v10, v85, v52
	v_fmac_f32_e32 v11, v86, v52
	v_fmac_f32_e32 v12, v87, v52
	v_fmac_f32_e32 v13, v88, v52
	v_cvt_f32_ubyte0_e32 v85, v23
	v_cvt_f32_ubyte1_e32 v86, v23
	v_cvt_f32_ubyte2_e32 v87, v23
	v_cvt_f32_ubyte3_e32 v88, v23
	v_fmac_f32_e32 v14, v85, v52
	v_fmac_f32_e32 v15, v86, v52
	v_fmac_f32_e32 v16, v87, v52
	v_fmac_f32_e32 v17, v88, v52
	s_waitcnt vmcnt(2)
	v_cvt_f32_ubyte0_e32 v85, v24
	v_cvt_f32_ubyte1_e32 v86, v24
	v_cvt_f32_ubyte2_e32 v87, v24
	v_cvt_f32_ubyte3_e32 v88, v24
	v_fmac_f32_e32 v2, v85, v53
	v_fmac_f32_e32 v3, v86, v53
	v_fmac_f32_e32 v4, v87, v53
	v_fmac_f32_e32 v5, v88, v53
	v_cvt_f32_ubyte0_e32 v85, v25
	v_cvt_f32_ubyte1_e32 v86, v25
	v_cvt_f32_ubyte2_e32 v87, v25
	v_cvt_f32_ubyte3_e32 v88, v25
	v_fmac_f32_e32 v6, v85, v53
	v_fmac_f32_e32 v7, v86, v53
	v_fmac_f32_e32 v8, v87, v53
	v_fmac_f32_e32 v9, v88, v53
	v_cvt_f32_ubyte0_e32 v85, v26
	v_cvt_f32_ubyte1_e32 v86, v26
	v_cvt_f32_ubyte2_e32 v87, v26
	v_cvt_f32_ubyte3_e32 v88, v26
	v_fmac_f32_e32 v10, v85, v53
	v_fmac_f32_e32 v11, v86, v53
	v_fmac_f32_e32 v12, v87, v53
	v_fmac_f32_e32 v13, v88, v53
	v_cvt_f32_ubyte0_e32 v85, v27
	v_cvt_f32_ubyte1_e32 v86, v27
	v_cvt_f32_ubyte2_e32 v87, v27
	v_cvt_f32_ubyte3_e32 v88, v27
	v_fmac_f32_e32 v14, v85, v53
	v_fmac_f32_e32 v15, v86, v53
	v_fmac_f32_e32 v16, v87, v53
	v_fmac_f32_e32 v17, v88, v53
	s_waitcnt vmcnt(1)
	v_cvt_f32_ubyte0_e32 v85, v28
	v_cvt_f32_ubyte1_e32 v86, v28
	v_cvt_f32_ubyte2_e32 v87, v28
	v_cvt_f32_ubyte3_e32 v88, v28
	v_fmac_f32_e32 v2, v85, v54
	v_fmac_f32_e32 v3, v86, v54
	v_fmac_f32_e32 v4, v87, v54
	v_fmac_f32_e32 v5, v88, v54
	v_cvt_f32_ubyte0_e32 v85, v29
	v_cvt_f32_ubyte1_e32 v86, v29
	v_cvt_f32_ubyte2_e32 v87, v29
	v_cvt_f32_ubyte3_e32 v88, v29
	v_fmac_f32_e32 v6, v85, v54
	v_fmac_f32_e32 v7, v86, v54
	v_fmac_f32_e32 v8, v87, v54
	v_fmac_f32_e32 v9, v88, v54
	v_cvt_f32_ubyte0_e32 v85, v30
	v_cvt_f32_ubyte1_e32 v86, v30
	v_cvt_f32_ubyte2_e32 v87, v30
	v_cvt_f32_ubyte3_e32 v88, v30
	v_fmac_f32_e32 v10, v85, v54
	v_fmac_f32_e32 v11, v86, v54
	v_fmac_f32_e32 v12, v87, v54
	v_fmac_f32_e32 v13, v88, v54
	v_cvt_f32_ubyte0_e32 v85, v31
	v_cvt_f32_ubyte1_e32 v86, v31
	v_cvt_f32_ubyte2_e32 v87, v31
	v_cvt_f32_ubyte3_e32 v88, v31
	v_fmac_f32_e32 v14, v85, v54
	v_fmac_f32_e32 v15, v86, v54
	v_fmac_f32_e32 v16, v87, v54
	v_fmac_f32_e32 v17, v88, v54
	s_waitcnt vmcnt(0)
	v_cvt_f32_ubyte0_e32 v85, v32
	v_cvt_f32_ubyte1_e32 v86, v32
	v_cvt_f32_ubyte2_e32 v87, v32
	v_cvt_f32_ubyte3_e32 v88, v32
	v_fmac_f32_e32 v2, v85, v55
	v_fmac_f32_e32 v3, v86, v55
	v_fmac_f32_e32 v4, v87, v55
	v_fmac_f32_e32 v5, v88, v55
	v_cvt_f32_ubyte0_e32 v85, v33
	v_cvt_f32_ubyte1_e32 v86, v33
	v_cvt_f32_ubyte2_e32 v87, v33
	v_cvt_f32_ubyte3_e32 v88, v33
	v_fmac_f32_e32 v6, v85, v55
	v_fmac_f32_e32 v7, v86, v55
	v_fmac_f32_e32 v8, v87, v55
	v_fmac_f32_e32 v9, v88, v55
	v_cvt_f32_ubyte0_e32 v85, v34
	v_cvt_f32_ubyte1_e32 v86, v34
	v_cvt_f32_ubyte2_e32 v87, v34
	v_cvt_f32_ubyte3_e32 v88, v34
	v_fmac_f32_e32 v10, v85, v55
	v_fmac_f32_e32 v11, v86, v55
	v_fmac_f32_e32 v12, v87, v55
	v_fmac_f32_e32 v13, v88, v55
	v_cvt_f32_ubyte0_e32 v85, v35
	v_cvt_f32_ubyte1_e32 v86, v35
	v_cvt_f32_ubyte2_e32 v87, v35
	v_cvt_f32_ubyte3_e32 v88, v35
	v_fmac_f32_e32 v14, v85, v55
	v_fmac_f32_e32 v15, v86, v55
	v_fmac_f32_e32 v16, v87, v55
	v_fmac_f32_e32 v17, v88, v55
.Lg2_rare_check:
	s_cmp_le_i32 s41, 32
	s_cbranch_scc1 .Lg2_final
	s_mov_b32 s42, 32
.Lg2_rare_loop:
	v_mov_b32_e32 v84, 0xc350
	v_cmp_lt_i32_e32 vcc, s42, v78
	v_add_u32_e32 v83, s42, v77
	v_lshlrev_b32_e32 v83, 2, v83
	s_and_saveexec_b64 s[44:45], vcc
	global_load_dword v84, v83, s[20:21]
	s_or_b64 exec, exec, s[44:45]
	s_waitcnt vmcnt(0)
	v_lshlrev_b32_e32 v83, 1, v84
	global_load_ushort v19, v83, s[14:15]
	v_lshl_or_b32 v83, v84, 7, v89
	global_load_dwordx4 v[20:23], v83, s[12:13]
	s_waitcnt vmcnt(0)
	v_cvt_f32_f16_e32 v19, v19
	v_cvt_f32_ubyte0_e32 v85, v20
	v_cvt_f32_ubyte1_e32 v86, v20
	v_cvt_f32_ubyte2_e32 v87, v20
	v_cvt_f32_ubyte3_e32 v88, v20
	v_fmac_f32_e32 v2, v85, v19
	v_fmac_f32_e32 v3, v86, v19
	v_fmac_f32_e32 v4, v87, v19
	v_fmac_f32_e32 v5, v88, v19
	v_cvt_f32_ubyte0_e32 v85, v21
	v_cvt_f32_ubyte1_e32 v86, v21
	v_cvt_f32_ubyte2_e32 v87, v21
	v_cvt_f32_ubyte3_e32 v88, v21
	v_fmac_f32_e32 v6, v85, v19
	v_fmac_f32_e32 v7, v86, v19
	v_fmac_f32_e32 v8, v87, v19
	v_fmac_f32_e32 v9, v88, v19
	v_cvt_f32_ubyte0_e32 v85, v22
	v_cvt_f32_ubyte1_e32 v86, v22
	v_cvt_f32_ubyte2_e32 v87, v22
	v_cvt_f32_ubyte3_e32 v88, v22
	v_fmac_f32_e32 v10, v85, v19
	v_fmac_f32_e32 v11, v86, v19
	v_fmac_f32_e32 v12, v87, v19
	v_fmac_f32_e32 v13, v88, v19
	v_cvt_f32_ubyte0_e32 v85, v23
	v_cvt_f32_ubyte1_e32 v86, v23
	v_cvt_f32_ubyte2_e32 v87, v23
	v_cvt_f32_ubyte3_e32 v88, v23
	v_fmac_f32_e32 v14, v85, v19
	v_fmac_f32_e32 v15, v86, v19
	v_fmac_f32_e32 v16, v87, v19
	v_fmac_f32_e32 v17, v88, v19
	s_add_i32 s42, s42, 1
	s_cmp_lt_i32 s42, s41
	s_cbranch_scc1 .Lg2_rare_loop
.Lg2_final:
	v_max_i32_e32 v94, 1, v78
	v_cvt_f32_u32_e32 v94, v94
	v_div_scale_f32 v96, s[62:63], v94, v94, 1.0
	v_rcp_f32_e32 v97, v96
	v_div_scale_f32 v98, vcc, 1.0, v94, 1.0
	v_fma_f32 v99, -v96, v97, 1.0
	v_fmac_f32_e32 v97, v99, v97
	v_mul_f32_e32 v99, v98, v97
	v_fma_f32 v95, -v96, v99, v98
	v_fmac_f32_e32 v99, v95, v97
	v_fma_f32 v96, -v96, v99, v98
	v_div_fmas_f32 v96, v96, v97, v99
	v_div_fixup_f32 v95, v96, v94, 1.0
	v_mul_f32_e32 v2, v95, v2
	v_mul_f32_e32 v3, v95, v3
	v_mul_f32_e32 v4, v95, v4
	v_mul_f32_e32 v5, v95, v5
	v_mul_f32_e32 v6, v95, v6
	v_mul_f32_e32 v7, v95, v7
	v_mul_f32_e32 v8, v95, v8
	v_mul_f32_e32 v9, v95, v9
	v_mul_f32_e32 v10, v95, v10
	v_mul_f32_e32 v11, v95, v11
	v_mul_f32_e32 v12, v95, v12
	v_mul_f32_e32 v13, v95, v13
	v_mul_f32_e32 v14, v95, v14
	v_mul_f32_e32 v15, v95, v15
	v_mul_f32_e32 v16, v95, v16
	v_mul_f32_e32 v17, v95, v17
	v_cvt_pk_f16_f32 v20, v2, v3
	v_cvt_pk_f16_f32 v21, v4, v5
	v_cvt_pk_f16_f32 v22, v6, v7
	v_cvt_pk_f16_f32 v23, v8, v9
	v_cvt_pk_f16_f32 v24, v10, v11
	v_cvt_pk_f16_f32 v25, v12, v13
	v_cvt_pk_f16_f32 v26, v14, v15
	v_cvt_pk_f16_f32 v27, v16, v17
	ds_write_b128 v93, v[20:23]
	ds_write_b128 v93, v[24:27] offset:16
	s_add_u32 s39, s39, 1
	s_cmp_lt_u32 s39, 2
	s_cbranch_scc1 .Lg2_set_top
	v_lshlrev_b32_e32 v107, 9, v105
	v_xor_b32_e32 v108, v106, v105
	v_lshlrev_b32_e32 v108, 4, v108
	v_mul_u32_u24_e32 v109, 0x110, v105
	v_lshl_add_u32 v109, v106, 4, v109
	v_add_u32_e32 v109, s48, v109
	v_lshlrev_b32_e32 v110, 4, v106
	v_add_u32_e32 v110, 0x10000, v110
	ds_read_b128 v[4:7], v110 offset:0
	ds_read_b128 v[8:11], v110 offset:64
	ds_read_b128 v[12:15], v110 offset:128
	ds_read_b128 v[16:19], v110 offset:192
	ds_read_b128 v[20:23], v110 offset:256
	ds_read_b128 v[24:27], v110 offset:320
	ds_read_b128 v[28:31], v110 offset:384
	ds_read_b128 v[32:35], v110 offset:448
	v_xor_b32_e32 v111, 0, v108
	v_add_u32_e32 v111, v111, v107
	ds_read_b128 v[100:103], v109
	ds_read_b128 v[36:39], v111 offset:0
	ds_read_b128 v[40:43], v111 offset:8192
	ds_read_b128 v[44:47], v111 offset:16384
	ds_read_b128 v[48:51], v111 offset:24576
	ds_read_b128 v[52:55], v111 offset:32768
	ds_read_b128 v[56:59], v111 offset:40960
	s_waitcnt lgkmcnt(7)
	ds_read_b128 v[60:63], v111 offset:49152
	ds_read_b128 v[64:67], v111 offset:57344
	s_waitcnt lgkmcnt(0)
	v_xor_b32_e32 v111, 64, v108
	v_add_u32_e32 v111, v111, v107
	ds_read_b128 v[0:3], v109 offset:64
	ds_read_b128 v[68:71], v111 offset:0
	ds_read_b128 v[72:75], v111 offset:8192
	ds_read_b128 v[76:79], v111 offset:16384
	ds_read_b128 v[80:83], v111 offset:24576
	ds_read_b128 v[84:87], v111 offset:32768
	ds_read_b128 v[88:91], v111 offset:40960
	ds_read_b128 v[92:95], v111 offset:49152
	ds_read_b128 v[96:99], v111 offset:57344
	v_mfma_f32_16x16x32_f16 v[4:7], v[36:39], v[100:103], v[4:7]
	v_mfma_f32_16x16x32_f16 v[8:11], v[40:43], v[100:103], v[8:11]
	v_mfma_f32_16x16x32_f16 v[12:15], v[44:47], v[100:103], v[12:15]
	v_mfma_f32_16x16x32_f16 v[16:19], v[48:51], v[100:103], v[16:19]
	v_mfma_f32_16x16x32_f16 v[20:23], v[52:55], v[100:103], v[20:23]
	v_mfma_f32_16x16x32_f16 v[24:27], v[56:59], v[100:103], v[24:27]
	v_mfma_f32_16x16x32_f16 v[28:31], v[60:63], v[100:103], v[28:31]
	v_mfma_f32_16x16x32_f16 v[32:35], v[64:67], v[100:103], v[32:35]
	s_waitcnt lgkmcnt(0)
	v_xor_b32_e32 v111, 128, v108
	v_add_u32_e32 v111, v111, v107
	ds_read_b128 v[100:103], v109 offset:128
	ds_read_b128 v[36:39], v111 offset:0
	ds_read_b128 v[40:43], v111 offset:8192
	ds_read_b128 v[44:47], v111 offset:16384
	ds_read_b128 v[48:51], v111 offset:24576
	ds_read_b128 v[52:55], v111 offset:32768
	ds_read_b128 v[56:59], v111 offset:40960
	ds_read_b128 v[60:63], v111 offset:49152
	ds_read_b128 v[64:67], v111 offset:57344
	v_mfma_f32_16x16x32_f16 v[4:7], v[68:71], v[0:3], v[4:7]
	v_mfma_f32_16x16x32_f16 v[8:11], v[72:75], v[0:3], v[8:11]
	v_mfma_f32_16x16x32_f16 v[12:15], v[76:79], v[0:3], v[12:15]
	v_mfma_f32_16x16x32_f16 v[16:19], v[80:83], v[0:3], v[16:19]
	v_mfma_f32_16x16x32_f16 v[20:23], v[84:87], v[0:3], v[20:23]
	v_mfma_f32_16x16x32_f16 v[24:27], v[88:91], v[0:3], v[24:27]
	v_mfma_f32_16x16x32_f16 v[28:31], v[92:95], v[0:3], v[28:31]
	v_mfma_f32_16x16x32_f16 v[32:35], v[96:99], v[0:3], v[32:35]
	s_waitcnt lgkmcnt(0)
	v_xor_b32_e32 v111, 192, v108
	v_add_u32_e32 v111, v111, v107
	ds_read_b128 v[0:3], v109 offset:192
	ds_read_b128 v[68:71], v111 offset:0
	ds_read_b128 v[72:75], v111 offset:8192
	ds_read_b128 v[76:79], v111 offset:16384
	ds_read_b128 v[80:83], v111 offset:24576
	ds_read_b128 v[84:87], v111 offset:32768
	ds_read_b128 v[88:91], v111 offset:40960
	ds_read_b128 v[92:95], v111 offset:49152
	ds_read_b128 v[96:99], v111 offset:57344
	v_mfma_f32_16x16x32_f16 v[4:7], v[36:39], v[100:103], v[4:7]
	v_mfma_f32_16x16x32_f16 v[8:11], v[40:43], v[100:103], v[8:11]
	v_mfma_f32_16x16x32_f16 v[12:15], v[44:47], v[100:103], v[12:15]
	v_mfma_f32_16x16x32_f16 v[16:19], v[48:51], v[100:103], v[16:19]
	v_mfma_f32_16x16x32_f16 v[20:23], v[52:55], v[100:103], v[20:23]
	v_mfma_f32_16x16x32_f16 v[24:27], v[56:59], v[100:103], v[24:27]
	v_mfma_f32_16x16x32_f16 v[28:31], v[60:63], v[100:103], v[28:31]
	v_mfma_f32_16x16x32_f16 v[32:35], v[64:67], v[100:103], v[32:35]
	s_waitcnt lgkmcnt(0)
	v_xor_b32_e32 v111, 256, v108
	v_add_u32_e32 v111, v111, v107
	ds_read_b128 v[36:39], v111 offset:0
	ds_read_b128 v[40:43], v111 offset:8192
	ds_read_b128 v[44:47], v111 offset:16384
	ds_read_b128 v[48:51], v111 offset:24576
	ds_read_b128 v[52:55], v111 offset:32768
	ds_read_b128 v[56:59], v111 offset:40960
	ds_read_b128 v[60:63], v111 offset:49152
	ds_read_b128 v[64:67], v111 offset:57344
	v_mfma_f32_16x16x32_f16 v[4:7], v[68:71], v[0:3], v[4:7]
	v_mfma_f32_16x16x32_f16 v[8:11], v[72:75], v[0:3], v[8:11]
	v_mfma_f32_16x16x32_f16 v[12:15], v[76:79], v[0:3], v[12:15]
	v_mfma_f32_16x16x32_f16 v[16:19], v[80:83], v[0:3], v[16:19]
	v_mfma_f32_16x16x32_f16 v[20:23], v[84:87], v[0:3], v[20:23]
	v_mfma_f32_16x16x32_f16 v[24:27], v[88:91], v[0:3], v[24:27]
	v_mfma_f32_16x16x32_f16 v[28:31], v[92:95], v[0:3], v[28:31]
	v_mfma_f32_16x16x32_f16 v[32:35], v[96:99], v[0:3], v[32:35]
	s_waitcnt lgkmcnt(0)
	s_waitcnt vmcnt(0)
	v_xor_b32_e32 v111, 320, v108
	v_add_u32_e32 v111, v111, v107
	ds_read_b128 v[68:71], v111 offset:0
	ds_read_b128 v[72:75], v111 offset:8192
	ds_read_b128 v[76:79], v111 offset:16384
	ds_read_b128 v[80:83], v111 offset:24576
	ds_read_b128 v[84:87], v111 offset:32768
	ds_read_b128 v[88:91], v111 offset:40960
	ds_read_b128 v[92:95], v111 offset:49152
	ds_read_b128 v[96:99], v111 offset:57344
	v_mfma_f32_16x16x32_f16 v[4:7], v[36:39], v[112:115], v[4:7]
	v_mfma_f32_16x16x32_f16 v[8:11], v[40:43], v[112:115], v[8:11]
	v_mfma_f32_16x16x32_f16 v[12:15], v[44:47], v[112:115], v[12:15]
	v_mfma_f32_16x16x32_f16 v[16:19], v[48:51], v[112:115], v[16:19]
	v_mfma_f32_16x16x32_f16 v[20:23], v[52:55], v[112:115], v[20:23]
	v_mfma_f32_16x16x32_f16 v[24:27], v[56:59], v[112:115], v[24:27]
	v_mfma_f32_16x16x32_f16 v[28:31], v[60:63], v[112:115], v[28:31]
	v_mfma_f32_16x16x32_f16 v[32:35], v[64:67], v[112:115], v[32:35]
	s_waitcnt lgkmcnt(0)
	v_xor_b32_e32 v111, 384, v108
	v_add_u32_e32 v111, v111, v107
	ds_read_b128 v[36:39], v111 offset:0
	ds_read_b128 v[40:43], v111 offset:8192
	ds_read_b128 v[44:47], v111 offset:16384
	ds_read_b128 v[48:51], v111 offset:24576
	ds_read_b128 v[52:55], v111 offset:32768
	ds_read_b128 v[56:59], v111 offset:40960
	ds_read_b128 v[60:63], v111 offset:49152
	ds_read_b128 v[64:67], v111 offset:57344
	v_mfma_f32_16x16x32_f16 v[4:7], v[68:71], v[116:119], v[4:7]
	v_mfma_f32_16x16x32_f16 v[8:11], v[72:75], v[116:119], v[8:11]
	v_mfma_f32_16x16x32_f16 v[12:15], v[76:79], v[116:119], v[12:15]
	v_mfma_f32_16x16x32_f16 v[16:19], v[80:83], v[116:119], v[16:19]
	v_mfma_f32_16x16x32_f16 v[20:23], v[84:87], v[116:119], v[20:23]
	v_mfma_f32_16x16x32_f16 v[24:27], v[88:91], v[116:119], v[24:27]
	v_mfma_f32_16x16x32_f16 v[28:31], v[92:95], v[116:119], v[28:31]
	v_mfma_f32_16x16x32_f16 v[32:35], v[96:99], v[116:119], v[32:35]
	s_waitcnt lgkmcnt(0)
	v_xor_b32_e32 v111, 448, v108
	v_add_u32_e32 v111, v111, v107
	ds_read_b128 v[68:71], v111 offset:0
	ds_read_b128 v[72:75], v111 offset:8192
	ds_read_b128 v[76:79], v111 offset:16384
	ds_read_b128 v[80:83], v111 offset:24576
	ds_read_b128 v[84:87], v111 offset:32768
	ds_read_b128 v[88:91], v111 offset:40960
	ds_read_b128 v[92:95], v111 offset:49152
	ds_read_b128 v[96:99], v111 offset:57344
	v_mfma_f32_16x16x32_f16 v[4:7], v[36:39], v[120:123], v[4:7]
	v_mfma_f32_16x16x32_f16 v[8:11], v[40:43], v[120:123], v[8:11]
	v_mfma_f32_16x16x32_f16 v[12:15], v[44:47], v[120:123], v[12:15]
	v_mfma_f32_16x16x32_f16 v[16:19], v[48:51], v[120:123], v[16:19]
	v_mfma_f32_16x16x32_f16 v[20:23], v[52:55], v[120:123], v[20:23]
	v_mfma_f32_16x16x32_f16 v[24:27], v[56:59], v[120:123], v[24:27]
	v_mfma_f32_16x16x32_f16 v[28:31], v[60:63], v[120:123], v[28:31]
	v_mfma_f32_16x16x32_f16 v[32:35], v[64:67], v[120:123], v[32:35]
	s_waitcnt lgkmcnt(0)
	v_mfma_f32_16x16x32_f16 v[4:7], v[68:71], v[124:127], v[4:7]
	v_mfma_f32_16x16x32_f16 v[8:11], v[72:75], v[124:127], v[8:11]
	v_mfma_f32_16x16x32_f16 v[12:15], v[76:79], v[124:127], v[12:15]
	v_mfma_f32_16x16x32_f16 v[16:19], v[80:83], v[124:127], v[16:19]
	v_mfma_f32_16x16x32_f16 v[20:23], v[84:87], v[124:127], v[20:23]
	v_mfma_f32_16x16x32_f16 v[24:27], v[88:91], v[124:127], v[24:27]
	v_mfma_f32_16x16x32_f16 v[28:31], v[92:95], v[124:127], v[28:31]
	v_mfma_f32_16x16x32_f16 v[32:35], v[96:99], v[124:127], v[32:35]
	s_nop 7
	s_nop 3
	v_mul_u32_u24_e32 v100, 0x110, v106
	v_lshl_add_u32 v100, v105, 4, v100
	v_add_u32_e32 v100, s48, v100
	v_lshlrev_b32_e32 v101, 2, v106
	v_lshlrev_b32_e32 v102, 4, v105
	ds_bpermute_b32 v68, v101, v104 offset:0
	ds_bpermute_b32 v69, v101, v104 offset:16
	ds_bpermute_b32 v70, v101, v104 offset:32
	ds_bpermute_b32 v71, v101, v104 offset:48
	ds_write_b128 v109, v[4:7] offset:0
	ds_write_b128 v109, v[8:11] offset:64
	ds_write_b128 v109, v[12:15] offset:128
	ds_write_b128 v109, v[16:19] offset:192
	ds_read_b128 v[36:39], v100 offset:0
	ds_read_b128 v[40:43], v100 offset:1088
	ds_read_b128 v[44:47], v100 offset:2176
	ds_read_b128 v[48:51], v100 offset:3264
	s_waitcnt lgkmcnt(3)
	v_lshl_or_b32 v68, v68, 9, v102
	global_store_dwordx4 v68, v[36:39], s[26:27] offset:0 sc1
	s_waitcnt lgkmcnt(2)
	v_lshl_or_b32 v69, v69, 9, v102
	global_store_dwordx4 v69, v[40:43], s[26:27] offset:0 sc1
	s_waitcnt lgkmcnt(1)
	v_lshl_or_b32 v70, v70, 9, v102
	global_store_dwordx4 v70, v[44:47], s[26:27] offset:0 sc1
	s_waitcnt lgkmcnt(0)
	v_lshl_or_b32 v71, v71, 9, v102
	global_store_dwordx4 v71, v[48:51], s[26:27] offset:0 sc1
	ds_write_b128 v109, v[20:23] offset:0
	ds_write_b128 v109, v[24:27] offset:64
	ds_write_b128 v109, v[28:31] offset:128
	ds_write_b128 v109, v[32:35] offset:192
	ds_read_b128 v[52:55], v100 offset:0
	ds_read_b128 v[56:59], v100 offset:1088
	ds_read_b128 v[60:63], v100 offset:2176
	ds_read_b128 v[64:67], v100 offset:3264
	s_waitcnt lgkmcnt(3)
	global_store_dwordx4 v68, v[52:55], s[26:27] offset:256 sc1
	s_waitcnt lgkmcnt(2)
	global_store_dwordx4 v69, v[56:59], s[26:27] offset:256 sc1
	s_waitcnt lgkmcnt(1)
	global_store_dwordx4 v70, v[60:63], s[26:27] offset:256 sc1
	s_waitcnt lgkmcnt(0)
	global_store_dwordx4 v71, v[64:67], s[26:27] offset:256 sc1
	s_endpgm
	.p2alignl 8, 3212836864

	.amdhsa_kernel _Z12layer_kernelILb0ELi0EEvPKfPKDF16_PKhS3_PK15HIP_vector_typeIiLj4EEPKtPKiS3_S1_PvPhPDF16_
		.amdhsa_group_segment_fixed_size 0
		.amdhsa_private_segment_fixed_size 0
		.amdhsa_kernarg_size 96
		.amdhsa_user_sgpr_count 2
		.amdhsa_user_sgpr_dispatch_ptr 0
		.amdhsa_user_sgpr_queue_ptr 0
		.amdhsa_user_sgpr_kernarg_segment_ptr 1
		.amdhsa_user_sgpr_dispatch_id 0
		.amdhsa_user_sgpr_kernarg_preload_length 0
		.amdhsa_user_sgpr_kernarg_preload_offset 0
		.amdhsa_user_sgpr_private_segment_size 0
		.amdhsa_uses_dynamic_stack 0
		.amdhsa_enable_private_segment 0
		.amdhsa_system_sgpr_workgroup_id_x 1
		.amdhsa_system_sgpr_workgroup_id_y 0
		.amdhsa_system_sgpr_workgroup_id_z 0
		.amdhsa_system_sgpr_workgroup_info 0
		.amdhsa_system_vgpr_workitem_id 0
		.amdhsa_next_free_vgpr 128
		.amdhsa_next_free_sgpr 64
		.amdhsa_accum_offset 128
		.amdhsa_reserve_vcc 1
		.amdhsa_float_round_mode_32 0
		.amdhsa_float_round_mode_16_64 0
		.amdhsa_float_denorm_mode_32 3
		.amdhsa_float_denorm_mode_16_64 3
		.amdhsa_dx10_clamp 1
		.amdhsa_ieee_mode 1
		.amdhsa_fp16_overflow 0
		.amdhsa_tg_split 0
		.amdhsa_exception_fp_ieee_invalid_op 0
		.amdhsa_exception_fp_denorm_src 0
		.amdhsa_exception_fp_ieee_div_zero 0
		.amdhsa_exception_fp_ieee_overflow 0
		.amdhsa_exception_fp_ieee_underflow 0
		.amdhsa_exception_fp_ieee_inexact 0
		.amdhsa_exception_int_div_zero 0
	.end_amdhsa_kernel

amdhsa.kernels:
  - .agpr_count:     0
    .args:
      - .actual_access:  read_only
        .address_space:  global
        .offset:         0
        .size:           8
        .value_kind:     global_buffer
      - .actual_access:  read_only
        .address_space:  global
        .offset:         8
        .size:           8
        .value_kind:     global_buffer
      - .actual_access:  read_only
        .address_space:  global
        .offset:         16
        .size:           8
        .value_kind:     global_buffer
      - .actual_access:  read_only
        .address_space:  global
        .offset:         24
        .size:           8
        .value_kind:     global_buffer
      - .actual_access:  read_only
        .address_space:  global
        .offset:         32
        .size:           8
        .value_kind:     global_buffer
      - .actual_access:  read_only
        .address_space:  global
        .offset:         40
        .size:           8
        .value_kind:     global_buffer
      - .actual_access:  read_only
        .address_space:  global
        .offset:         48
        .size:           8
        .value_kind:     global_buffer
      - .actual_access:  read_only
        .address_space:  global
        .offset:         56
        .size:           8
        .value_kind:     global_buffer
      - .actual_access:  write_only
        .address_space:  global
        .offset:         64
        .size:           8
        .value_kind:     global_buffer
      - .actual_access:  write_only
        .address_space:  global
        .offset:         72
        .size:           8
        .value_kind:     global_buffer
      - .actual_access:  write_only
        .address_space:  global
        .offset:         80
        .size:           8
        .value_kind:     global_buffer
      - .actual_access:  write_only
        .address_space:  global
        .offset:         88
        .size:           8
        .value_kind:     global_buffer
      - .actual_access:  write_only
        .address_space:  global
        .offset:         96
        .size:           8
        .value_kind:     global_buffer
      - .actual_access:  write_only
        .address_space:  global
        .offset:         104
        .size:           8
        .value_kind:     global_buffer
      - .actual_access:  write_only
        .address_space:  global
        .offset:         112
        .size:           8
        .value_kind:     global_buffer
    .group_segment_fixed_size: 14560
    .kernarg_segment_align: 8
    .kernarg_segment_size: 120
    .language:       OpenCL C
    .language_version:
      - 2
      - 0
    .max_flat_workgroup_size: 1024
    .name:           _Z12sort1_kernelPKfPKiS0_S0_S0_S0_PDF16_S3_S3_S3_PiPjPhS3_S3_
    .private_segment_fixed_size: 0
    .sgpr_count:     26
    .sgpr_spill_count: 0
    .symbol:         _Z12sort1_kernelPKfPKiS0_S0_S0_S0_PDF16_S3_S3_S3_PiPjPhS3_S3_.kd
    .uniform_work_group_size: 1
    .uses_dynamic_stack: false
    .vgpr_count:     31
    .vgpr_spill_count: 0
    .wavefront_size: 64
  - .agpr_count:     0
    .args:
      - .actual_access:  read_only
        .address_space:  global
        .offset:         0
        .size:           8
        .value_kind:     global_buffer
      - .actual_access:  read_only
        .address_space:  global
        .offset:         8
        .size:           8
        .value_kind:     global_buffer
      - .actual_access:  write_only
        .address_space:  global
        .offset:         16
        .size:           8
        .value_kind:     global_buffer
      - .actual_access:  write_only
        .address_space:  global
        .offset:         24
        .size:           8
        .value_kind:     global_buffer
      - .actual_access:  read_only
        .address_space:  global
        .offset:         32
        .size:           8
        .value_kind:     global_buffer
      - .actual_access:  read_only
        .address_space:  global
        .offset:         40
        .size:           8
        .value_kind:     global_buffer
      - .actual_access:  write_only
        .address_space:  global
        .offset:         48
        .size:           8
        .value_kind:     global_buffer
      - .actual_access:  write_only
        .address_space:  global
        .offset:         56
        .size:           8
        .value_kind:     global_buffer
      - .actual_access:  write_only
        .address_space:  global
        .offset:         64
        .size:           8
        .value_kind:     global_buffer
    .group_segment_fixed_size: 21792
    .kernarg_segment_align: 8
    .kernarg_segment_size: 72
    .language:       OpenCL C
    .language_version:
      - 2
      - 0
    .max_flat_workgroup_size: 1024
    .name:           _Z12sort2_kernelPKfPDF16_PhS1_PKiPKjP15HIP_vector_typeIiLj4EEPiPt
    .private_segment_fixed_size: 0
    .sgpr_count:     48
    .sgpr_spill_count: 0
    .symbol:         _Z12sort2_kernelPKfPDF16_PhS1_PKiPKjP15HIP_vector_typeIiLj4EEPiPt.kd
    .uniform_work_group_size: 1
    .uses_dynamic_stack: false
    .vgpr_count:     33
    .vgpr_spill_count: 0
    .wavefront_size: 64
  - .agpr_count:     0
    .args:
      - .actual_access:  read_only
        .address_space:  global
        .offset:         0
        .size:           8
        .value_kind:     global_buffer
      - .actual_access:  read_only
        .address_space:  global
        .offset:         8
        .size:           8
        .value_kind:     global_buffer
      - .actual_access:  read_only
        .address_space:  global
        .offset:         16
        .size:           8
        .value_kind:     global_buffer
      - .actual_access:  read_only
        .address_space:  global
        .offset:         24
        .size:           8
        .value_kind:     global_buffer
      - .actual_access:  read_only
        .address_space:  global
        .offset:         32
        .size:           8
        .value_kind:     global_buffer
      - .actual_access:  read_only
        .address_space:  global
        .offset:         40
        .size:           8
        .value_kind:     global_buffer
      - .actual_access:  read_only
        .address_space:  global
        .offset:         48
        .size:           8
        .value_kind:     global_buffer
      - .actual_access:  read_only
        .address_space:  global
        .offset:         56
        .size:           8
        .value_kind:     global_buffer
      - .actual_access:  read_only
        .address_space:  global
        .offset:         64
        .size:           8
        .value_kind:     global_buffer
      - .actual_access:  write_only
        .address_space:  global
        .offset:         72
        .size:           8
        .value_kind:     global_buffer
      - .actual_access:  write_only
        .address_space:  global
        .offset:         80
        .size:           8
        .value_kind:     global_buffer
      - .actual_access:  write_only
        .address_space:  global
        .offset:         88
        .size:           8
        .value_kind:     global_buffer
    .group_segment_fixed_size: 0
    .kernarg_segment_align: 8
    .kernarg_segment_size: 96
    .language:       OpenCL C
    .language_version:
      - 2
      - 0
    .max_flat_workgroup_size: 1024
    .name:           _Z12layer_kernelILb1ELi128EEvPKfPKDF16_PKhS3_PK15HIP_vector_typeIiLj4EEPKtPKiS3_S1_PvPhPDF16_
    .private_segment_fixed_size: 0
    .sgpr_count:     30
    .sgpr_spill_count: 0
    .symbol:         _Z12layer_kernelILb1ELi128EEvPKfPKDF16_PKhS3_PK15HIP_vector_typeIiLj4EEPKtPKiS3_S1_PvPhPDF16_.kd
    .uniform_work_group_size: 1
    .uses_dynamic_stack: false
    .vgpr_count:     110
    .vgpr_spill_count: 0
    .wavefront_size: 64
  - .agpr_count:     0
    .args:
      - .actual_access:  read_only
        .address_space:  global
        .offset:         0
        .size:           8
        .value_kind:     global_buffer
      - .actual_access:  read_only
        .address_space:  global
        .offset:         8
        .size:           8
        .value_kind:     global_buffer
      - .actual_access:  read_only
        .address_space:  global
        .offset:         16
        .size:           8
        .value_kind:     global_buffer
      - .actual_access:  read_only
        .address_space:  global
        .offset:         24
        .size:           8
        .value_kind:     global_buffer
      - .actual_access:  read_only
        .address_space:  global
        .offset:         32
        .size:           8
        .value_kind:     global_buffer
      - .actual_access:  read_only
        .address_space:  global
        .offset:         40
        .size:           8
        .value_kind:     global_buffer
      - .actual_access:  read_only
        .address_space:  global
        .offset:         48
        .size:           8
        .value_kind:     global_buffer
      - .actual_access:  read_only
        .address_space:  global
        .offset:         56
        .size:           8
        .value_kind:     global_buffer
      - .actual_access:  read_only
        .address_space:  global
        .offset:         64
        .size:           8
        .value_kind:     global_buffer
      - .actual_access:  write_only
        .address_space:  global
        .offset:         72
        .size:           8
        .value_kind:     global_buffer
      - .actual_access:  read_only
        .address_space:  global
        .offset:         80
        .size:           8
        .value_kind:     global_buffer
      - .actual_access:  read_only
        .address_space:  global
        .offset:         88
        .size:           8
        .value_kind:     global_buffer
    .group_segment_fixed_size: 0
    .kernarg_segment_align: 8
    .kernarg_segment_size: 96
    .language:       OpenCL C
    .language_version:
      - 2
      - 0
    .max_flat_workgroup_size: 1024
    .name:           _Z12layer_kernelILb0ELi0EEvPKfPKDF16_PKhS3_PK15HIP_vector_typeIiLj4EEPKtPKiS3_S1_PvPhPDF16_
    .private_segment_fixed_size: 0
    .sgpr_count:     70
    .sgpr_spill_count: 0
    .symbol:         _Z12layer_kernelILb0ELi0EEvPKfPKDF16_PKhS3_PK15HIP_vector_typeIiLj4EEPKtPKiS3_S1_PvPhPDF16_.kd
    .uniform_work_group_size: 1
    .uses_dynamic_stack: false
    .vgpr_count:     128
    .vgpr_spill_count: 0
    .wavefront_size: 64
